# Static priority: one s_setprio 1 for waves 4-7 at each GEMM K-loop entry (reset at exit), all per-MFMA-block priority flips in the four K-loops deleted
# speedup vs baseline: 1.0060x; 1.0060x over previous
.LBB0_166:
	s_ashr_i32 s45, s44, 31
	s_lshl_b64 s[48:49], s[44:45], 20
	s_add_u32 s48, s58, s48
	s_addc_u32 s49, s59, s49
	s_and_b64 s[50:51], s[26:27], exec
	s_cselect_b32 s7, s49, s55
	s_cselect_b32 s33, s48, s54
	s_ashr_i32 s47, s46, 31
	s_lshl_b64 s[50:51], s[46:47], 20
	s_add_u32 s50, s34, s50
	s_addc_u32 s51, s35, s51
	s_and_b64 s[56:57], s[26:27], exec
	s_cselect_b32 s45, s51, s5
	s_cselect_b32 s47, s50, s4
	s_add_u32 s54, s54, 0x80080
	s_addc_u32 s55, s55, 0
	s_add_u32 s79, s4, 0x100
	v_mov_b32_e32 v14, 0
	s_addc_u32 s80, s5, 0
	s_mov_b32 s81, -2
	v_mov_b32_e32 v15, v14
	v_mov_b32_e32 v16, v14
	v_mov_b32_e32 v17, v14
	s_waitcnt vmcnt(0)
	v_mov_b32_e32 v18, v14
	v_mov_b32_e32 v19, v14
	v_mov_b32_e32 v20, v14
	v_mov_b32_e32 v21, v14
	v_mov_b32_e32 v30, v14
	v_mov_b32_e32 v31, v14
	v_mov_b32_e32 v32, v14
	v_mov_b32_e32 v33, v14
	v_mov_b32_e32 v34, v14
	v_mov_b32_e32 v35, v14
	v_mov_b32_e32 v36, v14
	v_mov_b32_e32 v37, v14
	v_mov_b32_e32 v46, v14
	v_mov_b32_e32 v47, v14
	v_mov_b32_e32 v48, v14
	v_mov_b32_e32 v49, v14
	v_mov_b32_e32 v50, v14
	v_mov_b32_e32 v51, v14
	v_mov_b32_e32 v52, v14
	v_mov_b32_e32 v53, v14
	v_mov_b32_e32 v62, v14
	v_mov_b32_e32 v63, v14
	v_mov_b32_e32 v64, v14
	v_mov_b32_e32 v65, v14
	v_mov_b32_e32 v66, v14
	v_mov_b32_e32 v67, v14
	v_mov_b32_e32 v68, v14
	v_mov_b32_e32 v69, v14
	v_mov_b32_e32 v22, v14
	v_mov_b32_e32 v23, v14
	v_mov_b32_e32 v24, v14
	v_mov_b32_e32 v25, v14
	v_mov_b32_e32 v26, v14
	v_mov_b32_e32 v27, v14
	v_mov_b32_e32 v28, v14
	v_mov_b32_e32 v29, v14
	v_mov_b32_e32 v38, v14
	v_mov_b32_e32 v39, v14
	v_mov_b32_e32 v40, v14
	v_mov_b32_e32 v41, v14
	v_mov_b32_e32 v42, v14
	v_mov_b32_e32 v43, v14
	v_mov_b32_e32 v44, v14
	v_mov_b32_e32 v45, v14
	v_mov_b32_e32 v54, v14
	v_mov_b32_e32 v55, v14
	v_mov_b32_e32 v56, v14
	v_mov_b32_e32 v57, v14
	v_mov_b32_e32 v58, v14
	v_mov_b32_e32 v59, v14
	v_mov_b32_e32 v60, v14
	v_mov_b32_e32 v61, v14
	v_mov_b32_e32 v70, v14
	v_mov_b32_e32 v71, v14
	v_mov_b32_e32 v72, v14
	v_mov_b32_e32 v73, v14
	v_mov_b32_e32 v74, v14
	v_mov_b32_e32 v75, v14
	v_mov_b32_e32 v76, v14
	v_mov_b32_e32 v77, v14
	v_mov_b32_e32 v78, v14
	v_mov_b32_e32 v79, v14
	v_mov_b32_e32 v80, v14
	v_mov_b32_e32 v81, v14
	v_mov_b32_e32 v82, v14
	v_mov_b32_e32 v83, v14
	v_mov_b32_e32 v84, v14
	v_mov_b32_e32 v85, v14
	v_mov_b32_e32 v94, v14
	v_mov_b32_e32 v95, v14
	v_mov_b32_e32 v96, v14
	v_mov_b32_e32 v97, v14
	v_mov_b32_e32 v98, v14
	v_mov_b32_e32 v99, v14
	v_mov_b32_e32 v100, v14
	v_mov_b32_e32 v101, v14
	v_mov_b32_e32 v110, v14
	v_mov_b32_e32 v111, v14
	v_mov_b32_e32 v112, v14
	v_mov_b32_e32 v113, v14
	v_mov_b32_e32 v114, v14
	v_mov_b32_e32 v115, v14
	v_mov_b32_e32 v116, v14
	v_mov_b32_e32 v117, v14
	v_mov_b32_e32 v126, v14
	v_mov_b32_e32 v127, v14
	v_mov_b32_e32 v128, v14
	v_mov_b32_e32 v129, v14
	v_mov_b32_e32 v130, v14
	v_mov_b32_e32 v131, v14
	v_mov_b32_e32 v132, v14
	v_mov_b32_e32 v133, v14
	v_mov_b32_e32 v86, v14
	v_mov_b32_e32 v87, v14
	v_mov_b32_e32 v88, v14
	v_mov_b32_e32 v89, v14
	v_mov_b32_e32 v90, v14
	v_mov_b32_e32 v91, v14
	v_mov_b32_e32 v92, v14
	v_mov_b32_e32 v93, v14
	v_mov_b32_e32 v102, v14
	v_mov_b32_e32 v103, v14
	v_mov_b32_e32 v104, v14
	v_mov_b32_e32 v105, v14
	v_mov_b32_e32 v106, v14
	v_mov_b32_e32 v107, v14
	v_mov_b32_e32 v108, v14
	v_mov_b32_e32 v109, v14
	v_mov_b32_e32 v118, v14
	v_mov_b32_e32 v119, v14
	v_mov_b32_e32 v120, v14
	v_mov_b32_e32 v121, v14
	v_mov_b32_e32 v122, v14
	v_mov_b32_e32 v123, v14
	v_mov_b32_e32 v124, v14
	v_mov_b32_e32 v125, v14
	v_mov_b32_e32 v134, v14
	v_mov_b32_e32 v135, v14
	v_mov_b32_e32 v136, v14
	v_mov_b32_e32 v137, v14
	v_mov_b32_e32 v138, v14
	v_mov_b32_e32 v139, v14
	v_mov_b32_e32 v140, v14
	v_mov_b32_e32 v141, v14
	v_readfirstlane_b32 s101, v0
	s_nop 3
	s_and_b32 s101, s101, 0x3ff
	s_lshr_b32 s101, s101, 6
	s_cmp_ge_u32 s101, 4
	s_cbranch_scc0 .Lprio_p1_done
	s_setprio 1

.LBB0_167:
	s_barrier
	s_waitcnt lgkmcnt(0)
	v_mfma_f32_16x16x32_bf16 v[138:141], v[158:161], v[198:201], v[138:141]
	v_mfma_f32_16x16x32_bf16 v[134:137], v[166:169], v[198:201], v[134:137]
	v_mfma_f32_16x16x32_bf16 v[122:125], v[158:161], v[190:193], v[122:125]
	v_mfma_f32_16x16x32_bf16 v[118:121], v[166:169], v[190:193], v[118:121]
	v_mfma_f32_16x16x32_bf16 v[106:109], v[158:161], v[182:185], v[106:109]
	v_mfma_f32_16x16x32_bf16 v[102:105], v[166:169], v[182:185], v[102:105]
	v_mfma_f32_16x16x32_bf16 v[90:93], v[158:161], v[174:177], v[90:93]
	v_mfma_f32_16x16x32_bf16 v[86:89], v[166:169], v[174:177], v[86:89]
	v_mfma_f32_16x16x32_bf16 v[138:141], v[162:165], v[202:205], v[138:141]
	v_mfma_f32_16x16x32_bf16 v[134:137], v[170:173], v[202:205], v[134:137]
	v_mfma_f32_16x16x32_bf16 v[122:125], v[162:165], v[194:197], v[122:125]
	v_mfma_f32_16x16x32_bf16 v[118:121], v[170:173], v[194:197], v[118:121]
	v_mfma_f32_16x16x32_bf16 v[106:109], v[162:165], v[186:189], v[106:109]
	v_mfma_f32_16x16x32_bf16 v[102:105], v[170:173], v[186:189], v[102:105]
	v_mfma_f32_16x16x32_bf16 v[90:93], v[162:165], v[178:181], v[90:93]
	v_mfma_f32_16x16x32_bf16 v[86:89], v[170:173], v[178:181], v[86:89]
	v_mfma_f32_16x16x32_bf16 v[130:133], v[142:145], v[198:201], v[130:133]
	v_mfma_f32_16x16x32_bf16 v[126:129], v[150:153], v[198:201], v[126:129]
	v_mfma_f32_16x16x32_bf16 v[114:117], v[142:145], v[190:193], v[114:117]
	v_mfma_f32_16x16x32_bf16 v[110:113], v[150:153], v[190:193], v[110:113]
	v_mfma_f32_16x16x32_bf16 v[98:101], v[142:145], v[182:185], v[98:101]
	v_mfma_f32_16x16x32_bf16 v[94:97], v[150:153], v[182:185], v[94:97]
	v_mfma_f32_16x16x32_bf16 v[82:85], v[142:145], v[174:177], v[82:85]
	v_mfma_f32_16x16x32_bf16 v[78:81], v[150:153], v[174:177], v[78:81]
	v_mfma_f32_16x16x32_bf16 v[130:133], v[146:149], v[202:205], v[130:133]
	v_mfma_f32_16x16x32_bf16 v[126:129], v[154:157], v[202:205], v[126:129]
	v_mfma_f32_16x16x32_bf16 v[114:117], v[146:149], v[194:197], v[114:117]
	v_mfma_f32_16x16x32_bf16 v[110:113], v[154:157], v[194:197], v[110:113]
	v_mfma_f32_16x16x32_bf16 v[98:101], v[146:149], v[186:189], v[98:101]
	v_mfma_f32_16x16x32_bf16 v[94:97], v[154:157], v[186:189], v[94:97]
	v_mfma_f32_16x16x32_bf16 v[82:85], v[146:149], v[178:181], v[82:85]
	v_mfma_f32_16x16x32_bf16 v[78:81], v[154:157], v[178:181], v[78:81]

.Lp1vg_wd_b2:
	s_waitcnt lgkmcnt(0)
	s_barrier
	s_waitcnt lgkmcnt(0)
	v_mfma_f32_16x16x32_bf16 v[74:77], v[158:161], v[174:177], v[74:77]
	v_mfma_f32_16x16x32_bf16 v[70:73], v[166:169], v[174:177], v[70:73]
	v_mfma_f32_16x16x32_bf16 v[58:61], v[158:161], v[182:185], v[58:61]
	v_mfma_f32_16x16x32_bf16 v[54:57], v[166:169], v[182:185], v[54:57]
	v_mfma_f32_16x16x32_bf16 v[42:45], v[158:161], v[190:193], v[42:45]
	v_mfma_f32_16x16x32_bf16 v[38:41], v[166:169], v[190:193], v[38:41]
	v_mfma_f32_16x16x32_bf16 v[26:29], v[158:161], v[198:201], v[26:29]
	v_mfma_f32_16x16x32_bf16 v[22:25], v[166:169], v[198:201], v[22:25]
	v_mfma_f32_16x16x32_bf16 v[74:77], v[162:165], v[178:181], v[74:77]
	v_mfma_f32_16x16x32_bf16 v[70:73], v[170:173], v[178:181], v[70:73]
	v_mfma_f32_16x16x32_bf16 v[58:61], v[162:165], v[186:189], v[58:61]
	v_mfma_f32_16x16x32_bf16 v[54:57], v[170:173], v[186:189], v[54:57]
	v_mfma_f32_16x16x32_bf16 v[42:45], v[162:165], v[194:197], v[42:45]
	v_mfma_f32_16x16x32_bf16 v[38:41], v[170:173], v[194:197], v[38:41]
	v_mfma_f32_16x16x32_bf16 v[26:29], v[162:165], v[202:205], v[26:29]
	v_mfma_f32_16x16x32_bf16 v[22:25], v[170:173], v[202:205], v[22:25]
	v_mfma_f32_16x16x32_bf16 v[66:69], v[142:145], v[174:177], v[66:69]
	v_mfma_f32_16x16x32_bf16 v[62:65], v[150:153], v[174:177], v[62:65]
	v_mfma_f32_16x16x32_bf16 v[50:53], v[142:145], v[182:185], v[50:53]
	v_mfma_f32_16x16x32_bf16 v[46:49], v[150:153], v[182:185], v[46:49]
	v_mfma_f32_16x16x32_bf16 v[34:37], v[142:145], v[190:193], v[34:37]
	v_mfma_f32_16x16x32_bf16 v[30:33], v[150:153], v[190:193], v[30:33]
	v_mfma_f32_16x16x32_bf16 v[18:21], v[142:145], v[198:201], v[18:21]
	v_mfma_f32_16x16x32_bf16 v[14:17], v[150:153], v[198:201], v[14:17]
	v_mfma_f32_16x16x32_bf16 v[66:69], v[146:149], v[178:181], v[66:69]
	v_mfma_f32_16x16x32_bf16 v[62:65], v[154:157], v[178:181], v[62:65]
	v_mfma_f32_16x16x32_bf16 v[50:53], v[146:149], v[186:189], v[50:53]
	v_mfma_f32_16x16x32_bf16 v[46:49], v[154:157], v[186:189], v[46:49]
	v_mfma_f32_16x16x32_bf16 v[34:37], v[146:149], v[194:197], v[34:37]
	v_mfma_f32_16x16x32_bf16 v[30:33], v[154:157], v[194:197], v[30:33]
	v_mfma_f32_16x16x32_bf16 v[18:21], v[146:149], v[202:205], v[18:21]
	v_mfma_f32_16x16x32_bf16 v[14:17], v[154:157], v[202:205], v[14:17]
	s_barrier
	s_add_i32 s81, s81, 2
	s_add_u32 s54, s54, 0x100
	s_addc_u32 s55, s55, 0
	s_add_u32 s79, s79, 0x100
	s_addc_u32 s80, s80, 0
	s_cmp_gt_u32 s81, 29
	s_cbranch_scc1 .LBB0_180

; #define PG8_LAS __attribute__((address_space(3)))
;     __device__ __forceinline__ void issue(PG8_LAS unsigned char* lds0, int j, int tid, int wid) const {
;         const float* s0; unsigned char* d; addr(j, tid, s0, d);
;         __builtin_amdgcn_global_load_lds((const unsigned*)s0, (PG8_LAS unsigned*)(lds0 + stage + wid * 1024), 16, 0, 2);
;         __builtin_amdgcn_global_load_lds((const unsigned*)(s0 + ntot), (PG8_LAS unsigned*)(lds0 + stage + 8192 + wid * 1024), 16, 0, 2);
;     }
;     __device__ __forceinline__ void read(v4i_t& t0, v4i_t& t1, int tid, unsigned ldsb) const {
;         asm volatile("ds_read_b128 %0, %1" : "=&v"(t0) : "v"(ldsb + stage + 16u * (unsigned)tid) : "memory");
;         asm volatile("ds_read_b128 %0, %1" : "=&v"(t1) : "v"(ldsb + stage + 8192u + 16u * (unsigned)tid) : "memory");
;     }
;     __device__ __forceinline__ void finish(v4i_t& t0, v4i_t& t1, int j, int tid) const {
;         asm volatile("" : "+v"(t0), "+v"(t1));
;         const float* s0; unsigned char* d; addr(j, tid, s0, d);
;         const f32x4 r0 = __builtin_bit_cast(f32x4, t0) * 64.f, r1 = __builtin_bit_cast(f32x4, t1) * 64.f;
;         int w0 = 0, w1 = 0; w0 = __builtin_amdgcn_cvt_pk_fp8_f32(r0[0], r1[0], w0, false); w0 = __builtin_amdgcn_cvt_pk_fp8_f32(r0[1], r1[1], w0, true);
;         w1 = __builtin_amdgcn_cvt_pk_fp8_f32(r0[2], r1[2], w1, false); w1 = __builtin_amdgcn_cvt_pk_fp8_f32(r0[3], r1[3], w1, true);
;         typedef int v2is __attribute__((ext_vector_type(2))); __builtin_nontemporal_store((v2is){w0, w1}, (v2is*)d);
.Lp1vg_wd_a1:
	s_waitcnt lgkmcnt(0)
	s_barrier
	s_cmp_lt_i32 s98, 0
	s_cbranch_scc1 .Lp1vg_mmslow_a
	s_cmpk_gt_i32 s77, 0x5f
	s_cbranch_scc1 .Lp1vg_mmslow_a
	s_waitcnt lgkmcnt(0)
	v_mfma_f32_16x16x32_bf16 v[138:141], v[158:161], v[198:201], v[138:141]
	s_add_i32 s4, s98, s68
	s_lshr_b32 s2, s4, 31
	s_add_i32 s2, s4, s2
	v_mfma_f32_16x16x32_bf16 v[134:137], v[166:169], v[198:201], v[134:137]
	s_ashr_i32 s5, s2, 1
	s_ashr_i32 s2, s2, 11
	s_and_b32 s3, s5, 0x3ff
	v_mfma_f32_16x16x32_bf16 v[122:125], v[158:161], v[190:193], v[122:125]
	s_ashr_i32 s56, s2, 31
	s_lshl_b32 s2, s2, 10
	v_pk_mul_f32 v[6:7], v[6:7], s[40:41] op_sel_hi:[1,0]
	v_mfma_f32_16x16x32_bf16 v[118:121], v[166:169], v[190:193], v[118:121]
	v_pk_mul_f32 v[8:9], v[8:9], s[40:41] op_sel_hi:[1,0]
	v_pk_mul_f32 v[10:11], v[10:11], s[40:41] op_sel_hi:[1,0]
	v_pk_mul_f32 v[12:13], v[12:13], s[40:41] op_sel_hi:[1,0]
	v_mfma_f32_16x16x32_bf16 v[106:109], v[158:161], v[182:185], v[106:109]
	s_or_b32 s2, s2, s3
	v_cvt_pk_fp8_f32 v6, v6, v10
	s_mul_hi_u32 s3, s2, 0x2100
	v_mfma_f32_16x16x32_bf16 v[102:105], v[166:169], v[182:185], v[102:105]
	s_mulk_i32 s56, 0x2100
	v_cvt_pk_fp8_f32 v6, v7, v11 op_sel:[0,0,1]
	s_add_i32 s3, s3, s56
	v_mfma_f32_16x16x32_bf16 v[90:93], v[158:161], v[174:177], v[90:93]
	s_mulk_i32 s2, 0x2100
	v_cvt_pk_fp8_f32 v7, v8, v12
	v_readlane_b32 s101, v251, 49
	v_mfma_f32_16x16x32_bf16 v[86:89], v[166:169], v[174:177], v[86:89]
	s_add_u32 s2, s101, s2
	v_readlane_b32 s101, v251, 31
	s_addc_u32 s3, s101, s3
	v_mfma_f32_16x16x32_bf16 v[138:141], v[162:165], v[202:205], v[138:141]
	v_cvt_pk_fp8_f32 v7, v9, v13 op_sel:[0,0,1]
	v_lshl_or_b32 v226, s4, 11, v208
	s_lshl_b32 s56, s5, 12
	v_mfma_f32_16x16x32_bf16 v[134:137], v[170:173], v[202:205], v[134:137]
	v_subrev_u32_e32 v4, s56, v226
	v_ashrrev_i32_e32 v5, 31, v4
	v_lshl_add_u64 v[4:5], v[4:5], 1, s[2:3]
	v_mfma_f32_16x16x32_bf16 v[122:125], v[162:165], v[194:197], v[122:125]
	global_store_dwordx2 v[4:5], v[6:7], off nt
	s_add_i32 s4, s77, s68
	s_lshr_b32 s2, s4, 31
	v_mfma_f32_16x16x32_bf16 v[118:121], v[170:173], v[194:197], v[118:121]
	s_add_i32 s2, s4, s2
	s_ashr_i32 s5, s2, 1
	s_ashr_i32 s2, s2, 11
	v_mfma_f32_16x16x32_bf16 v[106:109], v[162:165], v[186:189], v[106:109]
	s_ashr_i32 s3, s2, 31
	s_lshl_b64 s[2:3], s[2:3], 25
	v_readlane_b32 s82, v251, 36
	v_mfma_f32_16x16x32_bf16 v[102:105], v[170:173], v[186:189], v[102:105]
	v_readlane_b32 s83, v251, 37
	s_add_u32 s2, s82, s2
	s_addc_u32 s3, s83, s3
	v_mfma_f32_16x16x32_bf16 v[90:93], v[162:165], v[178:181], v[90:93]
	s_lshl_b32 s82, s5, 15
	s_and_b32 s82, s82, 0x1ff8000
	s_add_u32 s82, s2, s82
	s_addc_u32 s83, s3, 0
	v_mfma_f32_16x16x32_bf16 v[86:89], v[170:173], v[178:181], v[86:89]
	s_lshl_b32 s2, s5, 12
	s_lshl_b32 s3, s4, 11
	s_sub_i32 s2, s3, s2
	v_mfma_f32_16x16x32_bf16 v[130:133], v[142:145], v[198:201], v[130:133]
	s_ashr_i32 s3, s2, 31
	s_lshl_b64 s[2:3], s[2:3], 2
	s_add_u32 s2, s82, s2
	s_addc_u32 s3, s83, s3
	v_mfma_f32_16x16x32_bf16 v[126:129], v[150:153], v[198:201], v[126:129]
	v_lshlrev_b32_e32 v2, 2, v208
	v_lshl_add_u64 v[4:5], s[2:3], 0, v[2:3]
	v_lshl_add_u64 v[4:5], v[4:5], 0, s[42:43]
	v_mfma_f32_16x16x32_bf16 v[114:117], v[142:145], v[190:193], v[114:117]
	global_load_dwordx4 v[6:9], v2, s[2:3] nt
	global_load_dwordx4 v[10:13], v[4:5], off nt
	s_mov_b32 s100, 3
	v_mfma_f32_16x16x32_bf16 v[110:113], v[150:153], v[190:193], v[110:113]
	s_mov_b32 s98, s77
	s_add_i32 s77, s77, 1
	s_add_u32 s4, s54, 0xfff80080
	s_addc_u32 s5, s55, -1
	v_mfma_f32_16x16x32_bf16 v[98:101], v[142:145], v[182:185], v[98:101]
	s_cmp_eq_u32 s81, 28
	s_cselect_b32 s5, s7, s5
	s_cselect_b32 s4, s33, s4
	s_cselect_b32 s57, s45, s80
	s_cselect_b32 s56, s47, s79
	v_mfma_f32_16x16x32_bf16 v[94:97], v[150:153], v[182:185], v[94:97]
	v_mfma_f32_16x16x32_bf16 v[82:85], v[142:145], v[174:177], v[82:85]
	v_mfma_f32_16x16x32_bf16 v[78:81], v[150:153], v[174:177], v[78:81]
	v_mfma_f32_16x16x32_bf16 v[130:133], v[146:149], v[202:205], v[130:133]
	v_mfma_f32_16x16x32_bf16 v[126:129], v[154:157], v[202:205], v[126:129]
	v_mfma_f32_16x16x32_bf16 v[114:117], v[146:149], v[194:197], v[114:117]
	v_mfma_f32_16x16x32_bf16 v[110:113], v[154:157], v[194:197], v[110:113]
	v_mfma_f32_16x16x32_bf16 v[98:101], v[146:149], v[186:189], v[98:101]
	v_mfma_f32_16x16x32_bf16 v[94:97], v[154:157], v[186:189], v[94:97]
	v_mfma_f32_16x16x32_bf16 v[82:85], v[146:149], v[178:181], v[82:85]
	v_mfma_f32_16x16x32_bf16 v[78:81], v[154:157], v[178:181], v[78:81]
	s_branch .Lp1vg_mmjoin_a

.Lp1vg_ni_a:
	s_add_u32 s4, s54, 0xfff80080
	s_addc_u32 s5, s55, -1
	s_cmp_eq_u32 s81, 28
	s_cselect_b32 s5, s7, s5
	s_cselect_b32 s4, s33, s4
	s_cselect_b32 s57, s45, s80
	s_cselect_b32 s56, s47, s79
	s_waitcnt lgkmcnt(0)
	v_mfma_f32_16x16x32_bf16 v[138:141], v[158:161], v[198:201], v[138:141]
	v_mfma_f32_16x16x32_bf16 v[134:137], v[166:169], v[198:201], v[134:137]
	v_mfma_f32_16x16x32_bf16 v[122:125], v[158:161], v[190:193], v[122:125]
	v_mfma_f32_16x16x32_bf16 v[118:121], v[166:169], v[190:193], v[118:121]
	v_mfma_f32_16x16x32_bf16 v[106:109], v[158:161], v[182:185], v[106:109]
	v_mfma_f32_16x16x32_bf16 v[102:105], v[166:169], v[182:185], v[102:105]
	v_mfma_f32_16x16x32_bf16 v[90:93], v[158:161], v[174:177], v[90:93]
	v_mfma_f32_16x16x32_bf16 v[86:89], v[166:169], v[174:177], v[86:89]
	v_mfma_f32_16x16x32_bf16 v[138:141], v[162:165], v[202:205], v[138:141]
	v_mfma_f32_16x16x32_bf16 v[134:137], v[170:173], v[202:205], v[134:137]
	v_mfma_f32_16x16x32_bf16 v[122:125], v[162:165], v[194:197], v[122:125]
	v_mfma_f32_16x16x32_bf16 v[118:121], v[170:173], v[194:197], v[118:121]
	v_mfma_f32_16x16x32_bf16 v[106:109], v[162:165], v[186:189], v[106:109]
	v_mfma_f32_16x16x32_bf16 v[102:105], v[170:173], v[186:189], v[102:105]
	v_mfma_f32_16x16x32_bf16 v[90:93], v[162:165], v[178:181], v[90:93]
	v_mfma_f32_16x16x32_bf16 v[86:89], v[170:173], v[178:181], v[86:89]
	v_mfma_f32_16x16x32_bf16 v[130:133], v[142:145], v[198:201], v[130:133]
	v_mfma_f32_16x16x32_bf16 v[126:129], v[150:153], v[198:201], v[126:129]
	v_mfma_f32_16x16x32_bf16 v[114:117], v[142:145], v[190:193], v[114:117]
	v_mfma_f32_16x16x32_bf16 v[110:113], v[150:153], v[190:193], v[110:113]
	v_mfma_f32_16x16x32_bf16 v[98:101], v[142:145], v[182:185], v[98:101]
	v_mfma_f32_16x16x32_bf16 v[94:97], v[150:153], v[182:185], v[94:97]
	v_mfma_f32_16x16x32_bf16 v[82:85], v[142:145], v[174:177], v[82:85]
	v_mfma_f32_16x16x32_bf16 v[78:81], v[150:153], v[174:177], v[78:81]
	v_mfma_f32_16x16x32_bf16 v[130:133], v[146:149], v[202:205], v[130:133]
	v_mfma_f32_16x16x32_bf16 v[126:129], v[154:157], v[202:205], v[126:129]
	v_mfma_f32_16x16x32_bf16 v[114:117], v[146:149], v[194:197], v[114:117]
	v_mfma_f32_16x16x32_bf16 v[110:113], v[154:157], v[194:197], v[110:113]
	v_mfma_f32_16x16x32_bf16 v[98:101], v[146:149], v[186:189], v[98:101]
	v_mfma_f32_16x16x32_bf16 v[94:97], v[154:157], v[186:189], v[94:97]
	v_mfma_f32_16x16x32_bf16 v[82:85], v[146:149], v[178:181], v[82:85]
	v_mfma_f32_16x16x32_bf16 v[78:81], v[154:157], v[178:181], v[78:81]

.Lp1vg_wd_a2:
	s_waitcnt lgkmcnt(0)
	s_barrier
	s_waitcnt lgkmcnt(0)
	v_mfma_f32_16x16x32_bf16 v[74:77], v[158:161], v[174:177], v[74:77]
	v_mfma_f32_16x16x32_bf16 v[70:73], v[166:169], v[174:177], v[70:73]
	v_mfma_f32_16x16x32_bf16 v[58:61], v[158:161], v[182:185], v[58:61]
	v_mfma_f32_16x16x32_bf16 v[54:57], v[166:169], v[182:185], v[54:57]
	v_mfma_f32_16x16x32_bf16 v[42:45], v[158:161], v[190:193], v[42:45]
	v_mfma_f32_16x16x32_bf16 v[38:41], v[166:169], v[190:193], v[38:41]
	v_mfma_f32_16x16x32_bf16 v[26:29], v[158:161], v[198:201], v[26:29]
	v_mfma_f32_16x16x32_bf16 v[22:25], v[166:169], v[198:201], v[22:25]
	v_mfma_f32_16x16x32_bf16 v[74:77], v[162:165], v[178:181], v[74:77]
	v_mfma_f32_16x16x32_bf16 v[70:73], v[170:173], v[178:181], v[70:73]
	v_mfma_f32_16x16x32_bf16 v[58:61], v[162:165], v[186:189], v[58:61]
	v_mfma_f32_16x16x32_bf16 v[54:57], v[170:173], v[186:189], v[54:57]
	v_mfma_f32_16x16x32_bf16 v[42:45], v[162:165], v[194:197], v[42:45]
	v_mfma_f32_16x16x32_bf16 v[38:41], v[170:173], v[194:197], v[38:41]
	v_mfma_f32_16x16x32_bf16 v[26:29], v[162:165], v[202:205], v[26:29]
	v_mfma_f32_16x16x32_bf16 v[22:25], v[170:173], v[202:205], v[22:25]
	v_mfma_f32_16x16x32_bf16 v[66:69], v[142:145], v[174:177], v[66:69]
	v_mfma_f32_16x16x32_bf16 v[62:65], v[150:153], v[174:177], v[62:65]
	v_mfma_f32_16x16x32_bf16 v[50:53], v[142:145], v[182:185], v[50:53]
	v_mfma_f32_16x16x32_bf16 v[46:49], v[150:153], v[182:185], v[46:49]
	v_mfma_f32_16x16x32_bf16 v[34:37], v[142:145], v[190:193], v[34:37]
	v_mfma_f32_16x16x32_bf16 v[30:33], v[150:153], v[190:193], v[30:33]
	v_mfma_f32_16x16x32_bf16 v[18:21], v[142:145], v[198:201], v[18:21]
	v_mfma_f32_16x16x32_bf16 v[14:17], v[150:153], v[198:201], v[14:17]
	v_mfma_f32_16x16x32_bf16 v[66:69], v[146:149], v[178:181], v[66:69]
	v_mfma_f32_16x16x32_bf16 v[62:65], v[154:157], v[178:181], v[62:65]
	v_mfma_f32_16x16x32_bf16 v[50:53], v[146:149], v[186:189], v[50:53]
	v_mfma_f32_16x16x32_bf16 v[46:49], v[154:157], v[186:189], v[46:49]
	v_mfma_f32_16x16x32_bf16 v[34:37], v[146:149], v[194:197], v[34:37]
	v_mfma_f32_16x16x32_bf16 v[30:33], v[154:157], v[194:197], v[30:33]
	v_mfma_f32_16x16x32_bf16 v[18:21], v[146:149], v[202:205], v[18:21]
	v_mfma_f32_16x16x32_bf16 v[14:17], v[154:157], v[202:205], v[14:17]
	s_barrier
	v_add_u32_e32 v2, 0x18000, v209
	ds_read_b128 v[158:161], v2
	ds_read_b128 v[162:165], v2 offset:1024
	ds_read_b128 v[166:169], v2 offset:2048
	ds_read_b128 v[170:173], v2 offset:3072
	v_add_u32_e32 v2, 0x1c000, v209
	ds_read_b128 v[142:145], v2
	ds_read_b128 v[146:149], v2 offset:1024
	ds_read_b128 v[150:153], v2 offset:2048
	ds_read_b128 v[154:157], v2 offset:3072
	s_add_u32 s4, s4, 0x80000
	s_addc_u32 s5, s5, 0
	s_mov_b32 m0, s66
	v_lshl_add_u64 v[238:239], s[4:5], 0, v[210:211]
	ds_read_b128 v[198:201], v234 offset:32768
	ds_read_b128 v[202:205], v234 offset:33792
	ds_read_b128 v[190:193], v234 offset:34816
	ds_read_b128 v[194:197], v234 offset:35840
	ds_read_b128 v[182:185], v234 offset:36864
	ds_read_b128 v[186:189], v234 offset:37888
	ds_read_b128 v[174:177], v234 offset:38912
	ds_read_b128 v[178:181], v234 offset:39936
	global_load_lds_dwordx4 v[238:239], off
	v_lshl_add_u64 v[238:239], s[4:5], 0, v[214:215]
	s_mov_b32 m0, s67
	s_nop 0
	global_load_lds_dwordx4 v[238:239], off
	s_cmp_eq_u32 s100, 3
	s_cbranch_scc1 .Lp1vg_w11_b1
	s_cmp_eq_u32 s100, 2
	s_cbranch_scc1 .Lp1vg_wk2_b1
	s_waitcnt vmcnt(8)
	s_branch .Lp1vg_wd_b1

;     __device__ __forceinline__ void finish(v4i_t& t0, v4i_t& t1, int j, int tid) const {
;         asm volatile("" : "+v"(t0), "+v"(t1));
;         const float* s0; unsigned char* d; addr(j, tid, s0, d);
;         const f32x4 r0 = __builtin_bit_cast(f32x4, t0) * 64.f, r1 = __builtin_bit_cast(f32x4, t1) * 64.f;
;         int w0 = 0, w1 = 0; w0 = __builtin_amdgcn_cvt_pk_fp8_f32(r0[0], r1[0], w0, false); w0 = __builtin_amdgcn_cvt_pk_fp8_f32(r0[1], r1[1], w0, true);
;         w1 = __builtin_amdgcn_cvt_pk_fp8_f32(r0[2], r1[2], w1, false); w1 = __builtin_amdgcn_cvt_pk_fp8_f32(r0[3], r1[3], w1, true);
;         typedef int v2is __attribute__((ext_vector_type(2))); __builtin_nontemporal_store((v2is){w0, w1}, (v2is*)d);
.Lp1vg_wd_b1:
	s_waitcnt lgkmcnt(0)
	s_cmp_lt_i32 s99, 0
	s_cbranch_scc1 .Lp1vg_mmslow_b
	s_cmpk_gt_i32 s77, 0x5f
	s_cbranch_scc1 .Lp1vg_mmslow_b
	s_barrier
	s_waitcnt lgkmcnt(0)
	v_mfma_f32_16x16x32_bf16 v[138:141], v[158:161], v[198:201], v[138:141]
	s_add_i32 s4, s99, s68
	s_lshr_b32 s2, s4, 31
	s_add_i32 s2, s4, s2
	v_mfma_f32_16x16x32_bf16 v[134:137], v[166:169], v[198:201], v[134:137]
	s_ashr_i32 s5, s2, 1
	s_ashr_i32 s2, s2, 11
	s_and_b32 s3, s5, 0x3ff
	v_mfma_f32_16x16x32_bf16 v[122:125], v[158:161], v[190:193], v[122:125]
	s_ashr_i32 s82, s2, 31
	s_lshl_b32 s2, s2, 10
	v_pk_mul_f32 v[240:241], v[240:241], s[40:41] op_sel_hi:[1,0]
	v_mfma_f32_16x16x32_bf16 v[118:121], v[166:169], v[190:193], v[118:121]
	v_pk_mul_f32 v[242:243], v[242:243], s[40:41] op_sel_hi:[1,0]
	v_pk_mul_f32 v[244:245], v[244:245], s[40:41] op_sel_hi:[1,0]
	v_pk_mul_f32 v[246:247], v[246:247], s[40:41] op_sel_hi:[1,0]
	v_mfma_f32_16x16x32_bf16 v[106:109], v[158:161], v[182:185], v[106:109]
	s_or_b32 s2, s2, s3
	v_cvt_pk_fp8_f32 v240, v240, v244
	s_mul_hi_u32 s3, s2, 0x2100
	v_mfma_f32_16x16x32_bf16 v[102:105], v[166:169], v[182:185], v[102:105]
	s_mulk_i32 s82, 0x2100
	v_cvt_pk_fp8_f32 v240, v241, v245 op_sel:[0,0,1]
	s_add_i32 s3, s3, s82
	v_mfma_f32_16x16x32_bf16 v[90:93], v[158:161], v[174:177], v[90:93]
	s_mulk_i32 s2, 0x2100
	v_cvt_pk_fp8_f32 v241, v242, v246
	v_readlane_b32 s101, v251, 49
	v_mfma_f32_16x16x32_bf16 v[86:89], v[166:169], v[174:177], v[86:89]
	s_add_u32 s2, s101, s2
	v_readlane_b32 s101, v251, 31
	s_addc_u32 s3, s101, s3
	v_mfma_f32_16x16x32_bf16 v[138:141], v[162:165], v[202:205], v[138:141]
	v_cvt_pk_fp8_f32 v241, v243, v247 op_sel:[0,0,1]
	v_lshl_or_b32 v248, s4, 11, v208
	s_lshl_b32 s82, s5, 12
	v_mfma_f32_16x16x32_bf16 v[134:137], v[170:173], v[202:205], v[134:137]
	v_subrev_u32_e32 v238, s82, v248
	v_ashrrev_i32_e32 v239, 31, v238
	v_lshl_add_u64 v[238:239], v[238:239], 1, s[2:3]
	v_mfma_f32_16x16x32_bf16 v[122:125], v[162:165], v[194:197], v[122:125]
	global_store_dwordx2 v[238:239], v[240:241], off nt
	s_add_i32 s4, s77, s68
	s_lshr_b32 s2, s4, 31
	v_mfma_f32_16x16x32_bf16 v[118:121], v[170:173], v[194:197], v[118:121]
	s_add_i32 s2, s4, s2
	s_ashr_i32 s5, s2, 1
	s_ashr_i32 s2, s2, 11
	v_mfma_f32_16x16x32_bf16 v[106:109], v[162:165], v[186:189], v[106:109]
	s_ashr_i32 s3, s2, 31
	s_lshl_b64 s[2:3], s[2:3], 25
	v_readlane_b32 s84, v251, 36
	v_mfma_f32_16x16x32_bf16 v[102:105], v[170:173], v[186:189], v[102:105]
	v_readlane_b32 s85, v251, 37
	s_add_u32 s2, s84, s2
	s_addc_u32 s3, s85, s3
	v_mfma_f32_16x16x32_bf16 v[90:93], v[162:165], v[178:181], v[90:93]
	s_lshl_b32 s84, s5, 15
	s_and_b32 s84, s84, 0x1ff8000
	s_add_u32 s84, s2, s84
	s_addc_u32 s85, s3, 0
	v_mfma_f32_16x16x32_bf16 v[86:89], v[170:173], v[178:181], v[86:89]
	s_lshl_b32 s2, s5, 12
	s_lshl_b32 s3, s4, 11
	s_sub_i32 s2, s3, s2
	v_mfma_f32_16x16x32_bf16 v[130:133], v[142:145], v[198:201], v[130:133]
	s_ashr_i32 s3, s2, 31
	s_lshl_b64 s[2:3], s[2:3], 2
	s_add_u32 s2, s84, s2
	s_addc_u32 s3, s85, s3
	v_mfma_f32_16x16x32_bf16 v[126:129], v[150:153], v[198:201], v[126:129]
	v_lshlrev_b32_e32 v2, 2, v208
	v_lshl_add_u64 v[238:239], s[2:3], 0, v[2:3]
	v_lshl_add_u64 v[238:239], v[238:239], 0, s[42:43]
	v_mfma_f32_16x16x32_bf16 v[114:117], v[142:145], v[190:193], v[114:117]
	global_load_dwordx4 v[240:243], v2, s[2:3] nt
	global_load_dwordx4 v[244:247], v[238:239], off nt
	s_mov_b32 s100, 3
	v_mfma_f32_16x16x32_bf16 v[110:113], v[150:153], v[190:193], v[110:113]
	s_mov_b32 s99, s77
	s_add_i32 s77, s77, 1
	v_mfma_f32_16x16x32_bf16 v[98:101], v[142:145], v[182:185], v[98:101]
	v_mfma_f32_16x16x32_bf16 v[94:97], v[150:153], v[182:185], v[94:97]
	v_mfma_f32_16x16x32_bf16 v[82:85], v[142:145], v[174:177], v[82:85]
	v_mfma_f32_16x16x32_bf16 v[78:81], v[150:153], v[174:177], v[78:81]
	v_mfma_f32_16x16x32_bf16 v[130:133], v[146:149], v[202:205], v[130:133]
	v_mfma_f32_16x16x32_bf16 v[126:129], v[154:157], v[202:205], v[126:129]
	v_mfma_f32_16x16x32_bf16 v[114:117], v[146:149], v[194:197], v[114:117]
	v_mfma_f32_16x16x32_bf16 v[110:113], v[154:157], v[194:197], v[110:113]
	v_mfma_f32_16x16x32_bf16 v[98:101], v[146:149], v[186:189], v[98:101]
	v_mfma_f32_16x16x32_bf16 v[94:97], v[154:157], v[186:189], v[94:97]
	v_mfma_f32_16x16x32_bf16 v[82:85], v[146:149], v[178:181], v[82:85]
	v_mfma_f32_16x16x32_bf16 v[78:81], v[154:157], v[178:181], v[78:81]
	s_branch .Lp1vg_mmafter_b

.LBB0_180:
	s_setprio 0
	s_and_b64 vcc, exec, s[38:39]
	s_cbranch_vccz .LBB0_182
	s_barrier

.LBB0_534:
	s_ashr_i32 s11, s10, 31
	v_cmp_lt_i64_e32 vcc, s[16:17], v[218:219]
	s_lshl_b64 s[16:17], s[10:11], 20
	s_add_u32 s16, s38, s16
	s_addc_u32 s17, s39, s17
	s_and_b64 s[18:19], vcc, exec
	s_cselect_b32 s11, s17, s25
	s_cselect_b32 s56, s16, s24
	s_ashr_i32 s15, s14, 31
	s_lshl_b64 s[18:19], s[14:15], 20
	s_add_u32 s18, s30, s18
	s_addc_u32 s19, s31, s19
	s_and_b64 s[34:35], vcc, exec
	s_cselect_b32 s15, s19, s5
	s_cselect_b32 s57, s18, s4
	s_add_u32 s24, s24, 0x80080
	s_addc_u32 s25, s25, 0
	s_add_u32 s58, s4, 0x100
	v_mov_b32_e32 v14, 0
	s_addc_u32 s59, s5, 0
	s_mov_b32 s60, -2
	v_mov_b32_e32 v15, v14
	v_mov_b32_e32 v16, v14
	v_mov_b32_e32 v17, v14
	s_waitcnt vmcnt(0)
	v_mov_b32_e32 v18, v14
	v_mov_b32_e32 v19, v14
	v_mov_b32_e32 v20, v14
	v_mov_b32_e32 v21, v14
	v_mov_b32_e32 v22, v14
	v_mov_b32_e32 v23, v14
	v_mov_b32_e32 v24, v14
	v_mov_b32_e32 v25, v14
	v_mov_b32_e32 v34, v14
	v_mov_b32_e32 v35, v14
	v_mov_b32_e32 v36, v14
	v_mov_b32_e32 v37, v14
	v_mov_b32_e32 v38, v14
	v_mov_b32_e32 v39, v14
	v_mov_b32_e32 v40, v14
	v_mov_b32_e32 v41, v14
	v_mov_b32_e32 v50, v14
	v_mov_b32_e32 v51, v14
	v_mov_b32_e32 v52, v14
	v_mov_b32_e32 v53, v14
	v_mov_b32_e32 v54, v14
	v_mov_b32_e32 v55, v14
	v_mov_b32_e32 v56, v14
	v_mov_b32_e32 v57, v14
	v_mov_b32_e32 v66, v14
	v_mov_b32_e32 v67, v14
	v_mov_b32_e32 v68, v14
	v_mov_b32_e32 v69, v14
	v_mov_b32_e32 v26, v14
	v_mov_b32_e32 v27, v14
	v_mov_b32_e32 v28, v14
	v_mov_b32_e32 v29, v14
	v_mov_b32_e32 v30, v14
	v_mov_b32_e32 v31, v14
	v_mov_b32_e32 v32, v14
	v_mov_b32_e32 v33, v14
	v_mov_b32_e32 v42, v14
	v_mov_b32_e32 v43, v14
	v_mov_b32_e32 v44, v14
	v_mov_b32_e32 v45, v14
	v_mov_b32_e32 v46, v14
	v_mov_b32_e32 v47, v14
	v_mov_b32_e32 v48, v14
	v_mov_b32_e32 v49, v14
	v_mov_b32_e32 v58, v14
	v_mov_b32_e32 v59, v14
	v_mov_b32_e32 v60, v14
	v_mov_b32_e32 v61, v14
	v_mov_b32_e32 v62, v14
	v_mov_b32_e32 v63, v14
	v_mov_b32_e32 v64, v14
	v_mov_b32_e32 v65, v14
	v_mov_b32_e32 v70, v14
	v_mov_b32_e32 v71, v14
	v_mov_b32_e32 v72, v14
	v_mov_b32_e32 v73, v14
	v_mov_b32_e32 v74, v14
	v_mov_b32_e32 v75, v14
	v_mov_b32_e32 v76, v14
	v_mov_b32_e32 v77, v14
	v_mov_b32_e32 v78, v14
	v_mov_b32_e32 v79, v14
	v_mov_b32_e32 v80, v14
	v_mov_b32_e32 v81, v14
	v_mov_b32_e32 v82, v14
	v_mov_b32_e32 v83, v14
	v_mov_b32_e32 v84, v14
	v_mov_b32_e32 v85, v14
	v_mov_b32_e32 v86, v14
	v_mov_b32_e32 v87, v14
	v_mov_b32_e32 v88, v14
	v_mov_b32_e32 v89, v14
	v_mov_b32_e32 v98, v14
	v_mov_b32_e32 v99, v14
	v_mov_b32_e32 v100, v14
	v_mov_b32_e32 v101, v14
	v_mov_b32_e32 v102, v14
	v_mov_b32_e32 v103, v14
	v_mov_b32_e32 v104, v14
	v_mov_b32_e32 v105, v14
	v_mov_b32_e32 v114, v14
	v_mov_b32_e32 v115, v14
	v_mov_b32_e32 v116, v14
	v_mov_b32_e32 v117, v14
	v_mov_b32_e32 v118, v14
	v_mov_b32_e32 v119, v14
	v_mov_b32_e32 v120, v14
	v_mov_b32_e32 v121, v14
	v_mov_b32_e32 v130, v14
	v_mov_b32_e32 v131, v14
	v_mov_b32_e32 v132, v14
	v_mov_b32_e32 v133, v14
	v_mov_b32_e32 v90, v14
	v_mov_b32_e32 v91, v14
	v_mov_b32_e32 v92, v14
	v_mov_b32_e32 v93, v14
	v_mov_b32_e32 v94, v14
	v_mov_b32_e32 v95, v14
	v_mov_b32_e32 v96, v14
	v_mov_b32_e32 v97, v14
	v_mov_b32_e32 v106, v14
	v_mov_b32_e32 v107, v14
	v_mov_b32_e32 v108, v14
	v_mov_b32_e32 v109, v14
	v_mov_b32_e32 v110, v14
	v_mov_b32_e32 v111, v14
	v_mov_b32_e32 v112, v14
	v_mov_b32_e32 v113, v14
	v_mov_b32_e32 v122, v14
	v_mov_b32_e32 v123, v14
	v_mov_b32_e32 v124, v14
	v_mov_b32_e32 v125, v14
	v_mov_b32_e32 v126, v14
	v_mov_b32_e32 v127, v14
	v_mov_b32_e32 v128, v14
	v_mov_b32_e32 v129, v14
	v_mov_b32_e32 v134, v14
	v_mov_b32_e32 v135, v14
	v_mov_b32_e32 v136, v14
	v_mov_b32_e32 v137, v14
	v_mov_b32_e32 v138, v14
	v_mov_b32_e32 v139, v14
	v_mov_b32_e32 v140, v14
	v_mov_b32_e32 v141, v14
	v_readfirstlane_b32 s101, v0
	s_nop 3
	s_and_b32 s101, s101, 0x3ff
	s_lshr_b32 s101, s101, 6
	s_cmp_ge_u32 s101, 4
	s_cbranch_scc0 .Lprio_p4_done
	s_setprio 1

.LBB0_535:
	s_barrier
	s_waitcnt lgkmcnt(0)
	v_mfma_f32_16x16x32_bf16 v[138:141], v[158:161], v[198:201], v[138:141]
	v_mfma_f32_16x16x32_bf16 v[134:137], v[166:169], v[198:201], v[134:137]
	v_mfma_f32_16x16x32_bf16 v[126:129], v[158:161], v[190:193], v[126:129]
	v_mfma_f32_16x16x32_bf16 v[122:125], v[166:169], v[190:193], v[122:125]
	v_mfma_f32_16x16x32_bf16 v[110:113], v[158:161], v[182:185], v[110:113]
	v_mfma_f32_16x16x32_bf16 v[106:109], v[166:169], v[182:185], v[106:109]
	v_mfma_f32_16x16x32_bf16 v[94:97], v[158:161], v[174:177], v[94:97]
	v_mfma_f32_16x16x32_bf16 v[90:93], v[166:169], v[174:177], v[90:93]
	v_mfma_f32_16x16x32_bf16 v[138:141], v[162:165], v[202:205], v[138:141]
	v_mfma_f32_16x16x32_bf16 v[134:137], v[170:173], v[202:205], v[134:137]
	v_mfma_f32_16x16x32_bf16 v[126:129], v[162:165], v[194:197], v[126:129]
	v_mfma_f32_16x16x32_bf16 v[122:125], v[170:173], v[194:197], v[122:125]
	v_mfma_f32_16x16x32_bf16 v[110:113], v[162:165], v[186:189], v[110:113]
	v_mfma_f32_16x16x32_bf16 v[106:109], v[170:173], v[186:189], v[106:109]
	v_mfma_f32_16x16x32_bf16 v[94:97], v[162:165], v[178:181], v[94:97]
	v_mfma_f32_16x16x32_bf16 v[90:93], v[170:173], v[178:181], v[90:93]
	v_mfma_f32_16x16x32_bf16 v[130:133], v[142:145], v[198:201], v[130:133]
	v_mfma_f32_16x16x32_bf16 v[118:121], v[150:153], v[198:201], v[118:121]
	v_mfma_f32_16x16x32_bf16 v[114:117], v[142:145], v[190:193], v[114:117]
	v_mfma_f32_16x16x32_bf16 v[102:105], v[150:153], v[190:193], v[102:105]
	v_mfma_f32_16x16x32_bf16 v[98:101], v[142:145], v[182:185], v[98:101]
	v_mfma_f32_16x16x32_bf16 v[86:89], v[150:153], v[182:185], v[86:89]
	v_mfma_f32_16x16x32_bf16 v[82:85], v[142:145], v[174:177], v[82:85]
	v_mfma_f32_16x16x32_bf16 v[78:81], v[150:153], v[174:177], v[78:81]
	v_mfma_f32_16x16x32_bf16 v[130:133], v[146:149], v[202:205], v[130:133]
	v_mfma_f32_16x16x32_bf16 v[118:121], v[154:157], v[202:205], v[118:121]
	v_mfma_f32_16x16x32_bf16 v[114:117], v[146:149], v[194:197], v[114:117]
	v_mfma_f32_16x16x32_bf16 v[102:105], v[154:157], v[194:197], v[102:105]
	v_mfma_f32_16x16x32_bf16 v[98:101], v[146:149], v[186:189], v[98:101]
	v_mfma_f32_16x16x32_bf16 v[86:89], v[154:157], v[186:189], v[86:89]
	v_mfma_f32_16x16x32_bf16 v[82:85], v[146:149], v[178:181], v[82:85]
	v_mfma_f32_16x16x32_bf16 v[78:81], v[154:157], v[178:181], v[78:81]

.Lp4vg_wd_b2:
	s_waitcnt lgkmcnt(0)
	s_barrier
	s_waitcnt lgkmcnt(0)
	v_mfma_f32_16x16x32_bf16 v[74:77], v[158:161], v[174:177], v[74:77]
	v_mfma_f32_16x16x32_bf16 v[70:73], v[166:169], v[174:177], v[70:73]
	v_mfma_f32_16x16x32_bf16 v[62:65], v[158:161], v[182:185], v[62:65]
	v_mfma_f32_16x16x32_bf16 v[58:61], v[166:169], v[182:185], v[58:61]
	v_mfma_f32_16x16x32_bf16 v[46:49], v[158:161], v[190:193], v[46:49]
	v_mfma_f32_16x16x32_bf16 v[42:45], v[166:169], v[190:193], v[42:45]
	v_mfma_f32_16x16x32_bf16 v[30:33], v[158:161], v[198:201], v[30:33]
	v_mfma_f32_16x16x32_bf16 v[26:29], v[166:169], v[198:201], v[26:29]
	v_mfma_f32_16x16x32_bf16 v[74:77], v[162:165], v[178:181], v[74:77]
	v_mfma_f32_16x16x32_bf16 v[70:73], v[170:173], v[178:181], v[70:73]
	v_mfma_f32_16x16x32_bf16 v[62:65], v[162:165], v[186:189], v[62:65]
	v_mfma_f32_16x16x32_bf16 v[58:61], v[170:173], v[186:189], v[58:61]
	v_mfma_f32_16x16x32_bf16 v[46:49], v[162:165], v[194:197], v[46:49]
	v_mfma_f32_16x16x32_bf16 v[42:45], v[170:173], v[194:197], v[42:45]
	v_mfma_f32_16x16x32_bf16 v[30:33], v[162:165], v[202:205], v[30:33]
	v_mfma_f32_16x16x32_bf16 v[26:29], v[170:173], v[202:205], v[26:29]
	v_mfma_f32_16x16x32_bf16 v[66:69], v[142:145], v[174:177], v[66:69]
	v_mfma_f32_16x16x32_bf16 v[54:57], v[150:153], v[174:177], v[54:57]
	v_mfma_f32_16x16x32_bf16 v[50:53], v[142:145], v[182:185], v[50:53]
	v_mfma_f32_16x16x32_bf16 v[38:41], v[150:153], v[182:185], v[38:41]
	v_mfma_f32_16x16x32_bf16 v[34:37], v[142:145], v[190:193], v[34:37]
	v_mfma_f32_16x16x32_bf16 v[22:25], v[150:153], v[190:193], v[22:25]
	v_mfma_f32_16x16x32_bf16 v[18:21], v[142:145], v[198:201], v[18:21]
	v_mfma_f32_16x16x32_bf16 v[14:17], v[150:153], v[198:201], v[14:17]
	v_mfma_f32_16x16x32_bf16 v[66:69], v[146:149], v[178:181], v[66:69]
	v_mfma_f32_16x16x32_bf16 v[54:57], v[154:157], v[178:181], v[54:57]
	v_mfma_f32_16x16x32_bf16 v[50:53], v[146:149], v[186:189], v[50:53]
	v_mfma_f32_16x16x32_bf16 v[38:41], v[154:157], v[186:189], v[38:41]
	v_mfma_f32_16x16x32_bf16 v[34:37], v[146:149], v[194:197], v[34:37]
	v_mfma_f32_16x16x32_bf16 v[22:25], v[154:157], v[194:197], v[22:25]
	v_mfma_f32_16x16x32_bf16 v[18:21], v[146:149], v[202:205], v[18:21]
	v_mfma_f32_16x16x32_bf16 v[14:17], v[154:157], v[202:205], v[14:17]
	s_barrier
	s_add_i32 s60, s60, 2
	s_add_u32 s24, s24, 0x100
	s_addc_u32 s25, s25, 0
	s_add_u32 s58, s58, 0x100
	s_addc_u32 s59, s59, 0
	s_cmp_gt_u32 s60, 29
	s_cbranch_scc1 .LBB0_548

;     __device__ __forceinline__ void finish(v4i_t& t0, v4i_t& t1, int j, int tid) const {
;         asm volatile("" : "+v"(t0), "+v"(t1));
;         const float* s0; unsigned char* d; addr(j, tid, s0, d);
;         const f32x4 r0 = __builtin_bit_cast(f32x4, t0) * 64.f, r1 = __builtin_bit_cast(f32x4, t1) * 64.f;
;         int w0 = 0, w1 = 0; w0 = __builtin_amdgcn_cvt_pk_fp8_f32(r0[0], r1[0], w0, false); w0 = __builtin_amdgcn_cvt_pk_fp8_f32(r0[1], r1[1], w0, true);
;         w1 = __builtin_amdgcn_cvt_pk_fp8_f32(r0[2], r1[2], w1, false); w1 = __builtin_amdgcn_cvt_pk_fp8_f32(r0[3], r1[3], w1, true);
;         typedef int v2is __attribute__((ext_vector_type(2))); __builtin_nontemporal_store((v2is){w0, w1}, (v2is*)d);
.Lp4vg_wd_a1:
	s_waitcnt lgkmcnt(0)
	s_barrier
	s_cmp_lt_i32 s98, 0
	s_cbranch_scc1 .Lp4vg_mmslow_a
	s_cmp_gt_i32 s42, 31
	s_cbranch_scc1 .Lp4vg_mmslow_a
	s_waitcnt lgkmcnt(0)
	v_mfma_f32_16x16x32_bf16 v[138:141], v[158:161], v[198:201], v[138:141]
	s_add_i32 s22, s98, s47
	s_lshr_b32 s4, s22, 31
	s_add_i32 s4, s22, s4
	v_mfma_f32_16x16x32_bf16 v[134:137], v[166:169], v[198:201], v[134:137]
	s_ashr_i32 s23, s4, 1
	s_ashr_i32 s4, s4, 11
	s_and_b32 s5, s23, 0x3ff
	v_mfma_f32_16x16x32_bf16 v[126:129], v[158:161], v[190:193], v[126:129]
	s_ashr_i32 s34, s4, 31
	s_lshl_b32 s4, s4, 10
	v_pk_mul_f32 v[6:7], v[6:7], s[2:3] op_sel_hi:[1,0]
	v_mfma_f32_16x16x32_bf16 v[122:125], v[166:169], v[190:193], v[122:125]
	v_pk_mul_f32 v[8:9], v[8:9], s[2:3] op_sel_hi:[1,0]
	v_pk_mul_f32 v[10:11], v[10:11], s[2:3] op_sel_hi:[1,0]
	v_pk_mul_f32 v[12:13], v[12:13], s[2:3] op_sel_hi:[1,0]
	v_mfma_f32_16x16x32_bf16 v[110:113], v[158:161], v[182:185], v[110:113]
	s_or_b32 s4, s4, s5
	v_cvt_pk_fp8_f32 v6, v6, v10
	s_mul_hi_u32 s5, s4, 0x2100
	v_mfma_f32_16x16x32_bf16 v[106:109], v[166:169], v[182:185], v[106:109]
	s_mulk_i32 s34, 0x2100
	v_cvt_pk_fp8_f32 v6, v7, v11 op_sel:[0,0,1]
	s_add_i32 s5, s5, s34
	v_mfma_f32_16x16x32_bf16 v[94:97], v[158:161], v[174:177], v[94:97]
	s_mulk_i32 s4, 0x2100
	v_cvt_pk_fp8_f32 v7, v8, v12
	v_readlane_b32 s101, v251, 49
	v_mfma_f32_16x16x32_bf16 v[90:93], v[166:169], v[174:177], v[90:93]
	s_add_u32 s4, s101, s4
	v_readlane_b32 s101, v251, 31
	s_addc_u32 s5, s101, s5
	v_mfma_f32_16x16x32_bf16 v[138:141], v[162:165], v[202:205], v[138:141]
	v_cvt_pk_fp8_f32 v7, v9, v13 op_sel:[0,0,1]
	v_lshl_or_b32 v222, s22, 11, v208
	s_lshl_b32 s34, s23, 12
	v_mfma_f32_16x16x32_bf16 v[134:137], v[170:173], v[202:205], v[134:137]
	v_subrev_u32_e32 v4, s34, v222
	v_ashrrev_i32_e32 v5, 31, v4
	v_lshl_add_u64 v[4:5], v[4:5], 1, s[4:5]
	v_mfma_f32_16x16x32_bf16 v[126:129], v[162:165], v[194:197], v[126:129]
	global_store_dwordx2 v[4:5], v[6:7], off nt
	s_add_i32 s22, s42, s47
	s_lshr_b32 s4, s22, 31
	v_mfma_f32_16x16x32_bf16 v[122:125], v[170:173], v[194:197], v[122:125]
	s_add_i32 s4, s22, s4
	s_ashr_i32 s23, s4, 1
	s_ashr_i32 s4, s4, 11
	v_mfma_f32_16x16x32_bf16 v[110:113], v[162:165], v[186:189], v[110:113]
	s_ashr_i32 s5, s4, 31
	s_lshl_b64 s[4:5], s[4:5], 25
	v_readlane_b32 s34, v251, 36
	v_mfma_f32_16x16x32_bf16 v[106:109], v[170:173], v[186:189], v[106:109]
	v_readlane_b32 s35, v251, 37
	s_add_u32 s4, s34, s4
	s_addc_u32 s5, s35, s5
	v_mfma_f32_16x16x32_bf16 v[94:97], v[162:165], v[178:181], v[94:97]
	s_lshl_b32 s34, s23, 15
	s_and_b32 s34, s34, 0x1ff8000
	s_add_u32 s34, s4, s34
	s_addc_u32 s35, s5, 0
	v_mfma_f32_16x16x32_bf16 v[90:93], v[170:173], v[178:181], v[90:93]
	s_lshl_b32 s4, s23, 12
	s_lshl_b32 s5, s22, 11
	s_sub_i32 s4, s5, s4
	v_mfma_f32_16x16x32_bf16 v[130:133], v[142:145], v[198:201], v[130:133]
	s_ashr_i32 s5, s4, 31
	s_lshl_b64 s[4:5], s[4:5], 2
	s_add_u32 s4, s34, s4
	s_addc_u32 s5, s35, s5
	v_mfma_f32_16x16x32_bf16 v[118:121], v[150:153], v[198:201], v[118:121]
	v_lshlrev_b32_e32 v2, 2, v208
	v_lshl_add_u64 v[4:5], s[4:5], 0, v[2:3]
	v_lshl_add_u64 v[4:5], v[4:5], 0, s[8:9]
	v_mfma_f32_16x16x32_bf16 v[114:117], v[142:145], v[190:193], v[114:117]
	global_load_dwordx4 v[6:9], v2, s[4:5] nt
	global_load_dwordx4 v[10:13], v[4:5], off nt
	s_mov_b32 s100, 3
	v_mfma_f32_16x16x32_bf16 v[102:105], v[150:153], v[190:193], v[102:105]
	s_mov_b32 s98, s42
	s_add_i32 s42, s42, 1
	s_add_u32 s4, s24, 0xfff80080
	s_addc_u32 s5, s25, -1
	v_mfma_f32_16x16x32_bf16 v[98:101], v[142:145], v[182:185], v[98:101]
	s_cmp_eq_u32 s60, 28
	s_cselect_b32 s5, s11, s5
	s_cselect_b32 s4, s56, s4
	s_cselect_b32 s35, s15, s59
	s_cselect_b32 s34, s57, s58
	v_mfma_f32_16x16x32_bf16 v[86:89], v[150:153], v[182:185], v[86:89]
	v_mfma_f32_16x16x32_bf16 v[82:85], v[142:145], v[174:177], v[82:85]
	v_mfma_f32_16x16x32_bf16 v[78:81], v[150:153], v[174:177], v[78:81]
	v_mfma_f32_16x16x32_bf16 v[130:133], v[146:149], v[202:205], v[130:133]
	v_mfma_f32_16x16x32_bf16 v[118:121], v[154:157], v[202:205], v[118:121]
	v_mfma_f32_16x16x32_bf16 v[114:117], v[146:149], v[194:197], v[114:117]
	v_mfma_f32_16x16x32_bf16 v[102:105], v[154:157], v[194:197], v[102:105]
	v_mfma_f32_16x16x32_bf16 v[98:101], v[146:149], v[186:189], v[98:101]
	v_mfma_f32_16x16x32_bf16 v[86:89], v[154:157], v[186:189], v[86:89]
	v_mfma_f32_16x16x32_bf16 v[82:85], v[146:149], v[178:181], v[82:85]
	v_mfma_f32_16x16x32_bf16 v[78:81], v[154:157], v[178:181], v[78:81]
	s_branch .Lp4vg_mmjoin_a

.Lp4vg_ni_a:
	s_add_u32 s4, s24, 0xfff80080
	s_addc_u32 s5, s25, -1
	s_cmp_eq_u32 s60, 28
	s_cselect_b32 s5, s11, s5
	s_cselect_b32 s4, s56, s4
	s_cselect_b32 s35, s15, s59
	s_cselect_b32 s34, s57, s58
	s_waitcnt lgkmcnt(0)
	v_mfma_f32_16x16x32_bf16 v[138:141], v[158:161], v[198:201], v[138:141]
	v_mfma_f32_16x16x32_bf16 v[134:137], v[166:169], v[198:201], v[134:137]
	v_mfma_f32_16x16x32_bf16 v[126:129], v[158:161], v[190:193], v[126:129]
	v_mfma_f32_16x16x32_bf16 v[122:125], v[166:169], v[190:193], v[122:125]
	v_mfma_f32_16x16x32_bf16 v[110:113], v[158:161], v[182:185], v[110:113]
	v_mfma_f32_16x16x32_bf16 v[106:109], v[166:169], v[182:185], v[106:109]
	v_mfma_f32_16x16x32_bf16 v[94:97], v[158:161], v[174:177], v[94:97]
	v_mfma_f32_16x16x32_bf16 v[90:93], v[166:169], v[174:177], v[90:93]
	v_mfma_f32_16x16x32_bf16 v[138:141], v[162:165], v[202:205], v[138:141]
	v_mfma_f32_16x16x32_bf16 v[134:137], v[170:173], v[202:205], v[134:137]
	v_mfma_f32_16x16x32_bf16 v[126:129], v[162:165], v[194:197], v[126:129]
	v_mfma_f32_16x16x32_bf16 v[122:125], v[170:173], v[194:197], v[122:125]
	v_mfma_f32_16x16x32_bf16 v[110:113], v[162:165], v[186:189], v[110:113]
	v_mfma_f32_16x16x32_bf16 v[106:109], v[170:173], v[186:189], v[106:109]
	v_mfma_f32_16x16x32_bf16 v[94:97], v[162:165], v[178:181], v[94:97]
	v_mfma_f32_16x16x32_bf16 v[90:93], v[170:173], v[178:181], v[90:93]
	v_mfma_f32_16x16x32_bf16 v[130:133], v[142:145], v[198:201], v[130:133]
	v_mfma_f32_16x16x32_bf16 v[118:121], v[150:153], v[198:201], v[118:121]
	v_mfma_f32_16x16x32_bf16 v[114:117], v[142:145], v[190:193], v[114:117]
	v_mfma_f32_16x16x32_bf16 v[102:105], v[150:153], v[190:193], v[102:105]
	v_mfma_f32_16x16x32_bf16 v[98:101], v[142:145], v[182:185], v[98:101]
	v_mfma_f32_16x16x32_bf16 v[86:89], v[150:153], v[182:185], v[86:89]
	v_mfma_f32_16x16x32_bf16 v[82:85], v[142:145], v[174:177], v[82:85]
	v_mfma_f32_16x16x32_bf16 v[78:81], v[150:153], v[174:177], v[78:81]
	v_mfma_f32_16x16x32_bf16 v[130:133], v[146:149], v[202:205], v[130:133]
	v_mfma_f32_16x16x32_bf16 v[118:121], v[154:157], v[202:205], v[118:121]
	v_mfma_f32_16x16x32_bf16 v[114:117], v[146:149], v[194:197], v[114:117]
	v_mfma_f32_16x16x32_bf16 v[102:105], v[154:157], v[194:197], v[102:105]
	v_mfma_f32_16x16x32_bf16 v[98:101], v[146:149], v[186:189], v[98:101]
	v_mfma_f32_16x16x32_bf16 v[86:89], v[154:157], v[186:189], v[86:89]
	v_mfma_f32_16x16x32_bf16 v[82:85], v[146:149], v[178:181], v[82:85]
	v_mfma_f32_16x16x32_bf16 v[78:81], v[154:157], v[178:181], v[78:81]

.Lp4vg_wd_a2:
	s_waitcnt lgkmcnt(0)
	s_barrier
	s_waitcnt lgkmcnt(0)
	v_mfma_f32_16x16x32_bf16 v[74:77], v[158:161], v[174:177], v[74:77]
	v_mfma_f32_16x16x32_bf16 v[70:73], v[166:169], v[174:177], v[70:73]
	v_mfma_f32_16x16x32_bf16 v[62:65], v[158:161], v[182:185], v[62:65]
	v_mfma_f32_16x16x32_bf16 v[58:61], v[166:169], v[182:185], v[58:61]
	v_mfma_f32_16x16x32_bf16 v[46:49], v[158:161], v[190:193], v[46:49]
	v_mfma_f32_16x16x32_bf16 v[42:45], v[166:169], v[190:193], v[42:45]
	v_mfma_f32_16x16x32_bf16 v[30:33], v[158:161], v[198:201], v[30:33]
	v_mfma_f32_16x16x32_bf16 v[26:29], v[166:169], v[198:201], v[26:29]
	v_mfma_f32_16x16x32_bf16 v[74:77], v[162:165], v[178:181], v[74:77]
	v_mfma_f32_16x16x32_bf16 v[70:73], v[170:173], v[178:181], v[70:73]
	v_mfma_f32_16x16x32_bf16 v[62:65], v[162:165], v[186:189], v[62:65]
	v_mfma_f32_16x16x32_bf16 v[58:61], v[170:173], v[186:189], v[58:61]
	v_mfma_f32_16x16x32_bf16 v[46:49], v[162:165], v[194:197], v[46:49]
	v_mfma_f32_16x16x32_bf16 v[42:45], v[170:173], v[194:197], v[42:45]
	v_mfma_f32_16x16x32_bf16 v[30:33], v[162:165], v[202:205], v[30:33]
	v_mfma_f32_16x16x32_bf16 v[26:29], v[170:173], v[202:205], v[26:29]
	v_mfma_f32_16x16x32_bf16 v[66:69], v[142:145], v[174:177], v[66:69]
	v_mfma_f32_16x16x32_bf16 v[54:57], v[150:153], v[174:177], v[54:57]
	v_mfma_f32_16x16x32_bf16 v[50:53], v[142:145], v[182:185], v[50:53]
	v_mfma_f32_16x16x32_bf16 v[38:41], v[150:153], v[182:185], v[38:41]
	v_mfma_f32_16x16x32_bf16 v[34:37], v[142:145], v[190:193], v[34:37]
	v_mfma_f32_16x16x32_bf16 v[22:25], v[150:153], v[190:193], v[22:25]
	v_mfma_f32_16x16x32_bf16 v[18:21], v[142:145], v[198:201], v[18:21]
	v_mfma_f32_16x16x32_bf16 v[14:17], v[150:153], v[198:201], v[14:17]
	v_mfma_f32_16x16x32_bf16 v[66:69], v[146:149], v[178:181], v[66:69]
	v_mfma_f32_16x16x32_bf16 v[54:57], v[154:157], v[178:181], v[54:57]
	v_mfma_f32_16x16x32_bf16 v[50:53], v[146:149], v[186:189], v[50:53]
	v_mfma_f32_16x16x32_bf16 v[38:41], v[154:157], v[186:189], v[38:41]
	v_mfma_f32_16x16x32_bf16 v[34:37], v[146:149], v[194:197], v[34:37]
	v_mfma_f32_16x16x32_bf16 v[22:25], v[154:157], v[194:197], v[22:25]
	v_mfma_f32_16x16x32_bf16 v[18:21], v[146:149], v[202:205], v[18:21]
	v_mfma_f32_16x16x32_bf16 v[14:17], v[154:157], v[202:205], v[14:17]
	s_barrier
	v_add_u32_e32 v2, 0x18000, v1
	ds_read_b128 v[158:161], v2
	ds_read_b128 v[162:165], v2 offset:1024
	ds_read_b128 v[166:169], v2 offset:2048
	ds_read_b128 v[170:173], v2 offset:3072
	v_add_u32_e32 v2, 0x1c000, v1
	ds_read_b128 v[142:145], v2
	ds_read_b128 v[146:149], v2 offset:1024
	ds_read_b128 v[150:153], v2 offset:2048
	ds_read_b128 v[154:157], v2 offset:3072
	s_add_u32 s4, s4, 0x80000
	s_addc_u32 s5, s5, 0
	s_mov_b32 m0, s44
	v_lshl_add_u64 v[232:233], s[4:5], 0, v[210:211]
	ds_read_b128 v[198:201], v230 offset:32768
	ds_read_b128 v[202:205], v230 offset:33792
	ds_read_b128 v[190:193], v230 offset:34816
	ds_read_b128 v[194:197], v230 offset:35840
	ds_read_b128 v[182:185], v230 offset:36864
	ds_read_b128 v[186:189], v230 offset:37888
	ds_read_b128 v[174:177], v230 offset:38912
	ds_read_b128 v[178:181], v230 offset:39936
	global_load_lds_dwordx4 v[232:233], off
	v_lshl_add_u64 v[232:233], s[4:5], 0, v[212:213]
	s_mov_b32 m0, s46
	s_nop 0
	global_load_lds_dwordx4 v[232:233], off
	s_cmp_eq_u32 s100, 3
	s_cbranch_scc1 .Lp4vg_w11_b1
	s_cmp_eq_u32 s100, 2
	s_cbranch_scc1 .Lp4vg_wk2_b1
	s_waitcnt vmcnt(8)
	s_branch .Lp4vg_wd_b1

;     __device__ __forceinline__ void finish(v4i_t& t0, v4i_t& t1, int j, int tid) const {
;         asm volatile("" : "+v"(t0), "+v"(t1));
;         const float* s0; unsigned char* d; addr(j, tid, s0, d);
;         const f32x4 r0 = __builtin_bit_cast(f32x4, t0) * 64.f, r1 = __builtin_bit_cast(f32x4, t1) * 64.f;
;         int w0 = 0, w1 = 0; w0 = __builtin_amdgcn_cvt_pk_fp8_f32(r0[0], r1[0], w0, false); w0 = __builtin_amdgcn_cvt_pk_fp8_f32(r0[1], r1[1], w0, true);
;         w1 = __builtin_amdgcn_cvt_pk_fp8_f32(r0[2], r1[2], w1, false); w1 = __builtin_amdgcn_cvt_pk_fp8_f32(r0[3], r1[3], w1, true);
;         typedef int v2is __attribute__((ext_vector_type(2))); __builtin_nontemporal_store((v2is){w0, w1}, (v2is*)d);
.Lp4vg_wd_b1:
	s_waitcnt lgkmcnt(0)
	s_cmp_lt_i32 s99, 0
	s_cbranch_scc1 .Lp4vg_mmslow_b
	s_cmp_gt_i32 s42, 31
	s_cbranch_scc1 .Lp4vg_mmslow_b
	s_barrier
	s_waitcnt lgkmcnt(0)
	v_mfma_f32_16x16x32_bf16 v[138:141], v[158:161], v[198:201], v[138:141]
	s_add_i32 s22, s99, s47
	s_lshr_b32 s4, s22, 31
	s_add_i32 s4, s22, s4
	v_mfma_f32_16x16x32_bf16 v[134:137], v[166:169], v[198:201], v[134:137]
	s_ashr_i32 s23, s4, 1
	s_ashr_i32 s4, s4, 11
	s_and_b32 s5, s23, 0x3ff
	v_mfma_f32_16x16x32_bf16 v[126:129], v[158:161], v[190:193], v[126:129]
	s_ashr_i32 s61, s4, 31
	s_lshl_b32 s4, s4, 10
	v_pk_mul_f32 v[242:243], v[242:243], s[2:3] op_sel_hi:[1,0]
	v_mfma_f32_16x16x32_bf16 v[122:125], v[166:169], v[190:193], v[122:125]
	v_pk_mul_f32 v[244:245], v[244:245], s[2:3] op_sel_hi:[1,0]
	v_pk_mul_f32 v[246:247], v[246:247], s[2:3] op_sel_hi:[1,0]
	v_pk_mul_f32 v[248:249], v[248:249], s[2:3] op_sel_hi:[1,0]
	v_mfma_f32_16x16x32_bf16 v[110:113], v[158:161], v[182:185], v[110:113]
	s_or_b32 s4, s4, s5
	v_cvt_pk_fp8_f32 v242, v242, v246
	s_mul_hi_u32 s5, s4, 0x2100
	v_mfma_f32_16x16x32_bf16 v[106:109], v[166:169], v[182:185], v[106:109]
	s_mulk_i32 s61, 0x2100
	v_cvt_pk_fp8_f32 v242, v243, v247 op_sel:[0,0,1]
	s_add_i32 s5, s5, s61
	v_mfma_f32_16x16x32_bf16 v[94:97], v[158:161], v[174:177], v[94:97]
	s_mulk_i32 s4, 0x2100
	v_cvt_pk_fp8_f32 v243, v244, v248
	v_readlane_b32 s101, v251, 49
	v_mfma_f32_16x16x32_bf16 v[90:93], v[166:169], v[174:177], v[90:93]
	s_add_u32 s4, s101, s4
	v_readlane_b32 s101, v251, 31
	s_addc_u32 s5, s101, s5
	v_mfma_f32_16x16x32_bf16 v[138:141], v[162:165], v[202:205], v[138:141]
	v_cvt_pk_fp8_f32 v243, v245, v249 op_sel:[0,0,1]
	v_lshl_or_b32 v234, s22, 11, v208
	s_lshl_b32 s61, s23, 12
	v_mfma_f32_16x16x32_bf16 v[134:137], v[170:173], v[202:205], v[134:137]
	v_subrev_u32_e32 v232, s61, v234
	v_ashrrev_i32_e32 v233, 31, v232
	v_lshl_add_u64 v[232:233], v[232:233], 1, s[4:5]
	v_mfma_f32_16x16x32_bf16 v[126:129], v[162:165], v[194:197], v[126:129]
	global_store_dwordx2 v[232:233], v[242:243], off nt
	s_add_i32 s22, s42, s47
	s_lshr_b32 s4, s22, 31
	v_mfma_f32_16x16x32_bf16 v[122:125], v[170:173], v[194:197], v[122:125]
	s_add_i32 s4, s22, s4
	s_ashr_i32 s23, s4, 1
	s_ashr_i32 s4, s4, 11
	v_mfma_f32_16x16x32_bf16 v[110:113], v[162:165], v[186:189], v[110:113]
	s_ashr_i32 s5, s4, 31
	s_lshl_b64 s[4:5], s[4:5], 25
	v_readlane_b32 s64, v251, 36
	v_mfma_f32_16x16x32_bf16 v[106:109], v[170:173], v[186:189], v[106:109]
	v_readlane_b32 s65, v251, 37
	s_add_u32 s4, s64, s4
	s_addc_u32 s5, s65, s5
	v_mfma_f32_16x16x32_bf16 v[94:97], v[162:165], v[178:181], v[94:97]
	s_lshl_b32 s64, s23, 15
	s_and_b32 s64, s64, 0x1ff8000
	s_add_u32 s64, s4, s64
	s_addc_u32 s65, s5, 0
	v_mfma_f32_16x16x32_bf16 v[90:93], v[170:173], v[178:181], v[90:93]
	s_lshl_b32 s4, s23, 12
	s_lshl_b32 s5, s22, 11
	s_sub_i32 s4, s5, s4
	v_mfma_f32_16x16x32_bf16 v[130:133], v[142:145], v[198:201], v[130:133]
	s_ashr_i32 s5, s4, 31
	s_lshl_b64 s[4:5], s[4:5], 2
	s_add_u32 s4, s64, s4
	s_addc_u32 s5, s65, s5
	v_mfma_f32_16x16x32_bf16 v[118:121], v[150:153], v[198:201], v[118:121]
	v_lshlrev_b32_e32 v2, 2, v208
	v_lshl_add_u64 v[232:233], s[4:5], 0, v[2:3]
	v_lshl_add_u64 v[232:233], v[232:233], 0, s[8:9]
	v_mfma_f32_16x16x32_bf16 v[114:117], v[142:145], v[190:193], v[114:117]
	global_load_dwordx4 v[242:245], v2, s[4:5] nt
	global_load_dwordx4 v[246:249], v[232:233], off nt
	s_mov_b32 s100, 3
	v_mfma_f32_16x16x32_bf16 v[102:105], v[150:153], v[190:193], v[102:105]
	s_mov_b32 s99, s42
	s_add_i32 s42, s42, 1
	v_mfma_f32_16x16x32_bf16 v[98:101], v[142:145], v[182:185], v[98:101]
	v_mfma_f32_16x16x32_bf16 v[86:89], v[150:153], v[182:185], v[86:89]
	v_mfma_f32_16x16x32_bf16 v[82:85], v[142:145], v[174:177], v[82:85]
	v_mfma_f32_16x16x32_bf16 v[78:81], v[150:153], v[174:177], v[78:81]
	v_mfma_f32_16x16x32_bf16 v[130:133], v[146:149], v[202:205], v[130:133]
	v_mfma_f32_16x16x32_bf16 v[118:121], v[154:157], v[202:205], v[118:121]
	v_mfma_f32_16x16x32_bf16 v[114:117], v[146:149], v[194:197], v[114:117]
	v_mfma_f32_16x16x32_bf16 v[102:105], v[154:157], v[194:197], v[102:105]
	v_mfma_f32_16x16x32_bf16 v[98:101], v[146:149], v[186:189], v[98:101]
	v_mfma_f32_16x16x32_bf16 v[86:89], v[154:157], v[186:189], v[86:89]
	v_mfma_f32_16x16x32_bf16 v[82:85], v[146:149], v[178:181], v[82:85]
	v_mfma_f32_16x16x32_bf16 v[78:81], v[154:157], v[178:181], v[78:81]
	s_branch .Lp4vg_mmafter_b

;     __device__ __forceinline__ void operator()(const f32x4 (&acc)[2][2][4][2], const Unit& u, int wr, int wc, int fr, int fq) const {
;         const int row0 = u.pm * BM + wr * 64 + fr, col0 = u.cn * BM + wc * 32 + 4 * fq;
; #pragma unroll
;         for (int ai = 0; ai < 2; ++ai)
; #pragma unroll
;             for (int m = 0; m < 4; ++m) { const size_t off = (size_t)(row0 + ai * HALF + m * 16) * ldc + col0;
; #pragma unroll
;                 for (int bj = 0; bj < 2; ++bj)
; #pragma unroll
;                     for (int n = 0; n < 2; ++n) { const f32x4 b = *(const f32x4*)(base + off + bj * HALF + n * 16); *(f32x4*)(out + off + bj * HALF + n * 16) = acc[ai][bj][m][n] + b; } }
;     }
.LBB0_548:
	s_setprio 0
	v_mov_b32_e32 v2, v0
	s_lshl_b32 s5, s20, 8
	v_readfirstlane_b32 s4, v2
	s_ashr_i32 s11, s4, 2
	s_andn2_b32 s11, s11, 63
	s_lshr_b32 s4, s4, 1
	s_add_i32 s11, s11, s5
	s_lshl_b32 s5, s55, 8
	s_and_b32 s4, s4, 0x60
	v_and_or_b32 v146, v2, 15, s11
	s_or_b32 s4, s4, s5
	v_lshrrev_b32_e32 v2, 2, v2
	v_and_or_b32 v148, v2, 12, s4
	v_ashrrev_i32_e32 v147, 31, v146
	v_ashrrev_i32_e32 v149, 31, v148
	v_lshlrev_b64 v[4:5], 11, v[146:147]
	v_lshl_add_u64 v[4:5], v[4:5], 0, v[148:149]
	v_readlane_b32 s56, v251, 3
	v_lshlrev_b64 v[4:5], 2, v[4:5]
	v_readlane_b32 s57, v251, 4
	v_readlane_b32 s12, v251, 52
	v_readlane_b32 s13, v251, 53
	v_lshl_add_u64 v[150:151], s[56:57], 0, v[4:5]
	v_lshl_add_u64 v[152:153], s[12:13], 0, v[4:5]
	s_mov_b64 s[4:5], 0x100000
	s_and_b64 vcc, exec, s[6:7]
	v_readlane_b32 s58, v251, 5
	v_readlane_b32 s59, v251, 6
	v_readlane_b32 s60, v251, 7
	v_readlane_b32 s61, v251, 8
	v_readlane_b32 s62, v251, 9
	v_readlane_b32 s63, v251, 10
	v_readlane_b32 s64, v251, 11
	v_readlane_b32 s65, v251, 12
	v_readlane_b32 s66, v251, 13
	v_readlane_b32 s67, v251, 14
	v_readlane_b32 s68, v251, 15
	v_readlane_b32 s69, v251, 16
	v_readlane_b32 s70, v251, 17
	v_readlane_b32 s71, v251, 18
	s_add_u32 s4, s56, 0x0
	s_addc_u32 s5, s57, 0
	global_load_dwordx4 v[142:145], v4, s[4:5]
	global_load_dwordx4 v[146:149], v4, s[4:5] offset:64
	global_load_dwordx4 v[150:153], v4, s[4:5] offset:512
	global_load_dwordx4 v[154:157], v4, s[4:5] offset:576
	s_add_u32 s4, s56, 0x20000
	s_addc_u32 s5, s57, 0
	global_load_dwordx4 v[158:161], v4, s[4:5]
	global_load_dwordx4 v[162:165], v4, s[4:5] offset:64
	global_load_dwordx4 v[166:169], v4, s[4:5] offset:512
	global_load_dwordx4 v[170:173], v4, s[4:5] offset:576
	s_add_u32 s4, s56, 0x40000
	s_addc_u32 s5, s57, 0
	global_load_dwordx4 v[174:177], v4, s[4:5]
	global_load_dwordx4 v[178:181], v4, s[4:5] offset:64
	global_load_dwordx4 v[182:185], v4, s[4:5] offset:512
	global_load_dwordx4 v[186:189], v4, s[4:5] offset:576
	s_add_u32 s4, s56, 0x60000
	s_addc_u32 s5, s57, 0
	global_load_dwordx4 v[190:193], v4, s[4:5]
	global_load_dwordx4 v[194:197], v4, s[4:5] offset:64
	global_load_dwordx4 v[198:201], v4, s[4:5] offset:512
	global_load_dwordx4 v[202:205], v4, s[4:5] offset:576
	s_add_u32 s100, s12, 0x0
	s_addc_u32 s101, s13, 0
	s_add_u32 s4, s56, 0x100000
	s_addc_u32 s5, s57, 0
	s_waitcnt vmcnt(15)
	v_pk_add_f32 v[142:143], v[138:139], v[142:143]
	v_pk_add_f32 v[144:145], v[140:141], v[144:145]
	global_store_dwordx4 v4, v[142:145], s[100:101]
	global_load_dwordx4 v[138:141], v4, s[4:5]
	s_waitcnt vmcnt(16)
	v_pk_add_f32 v[146:147], v[134:135], v[146:147]
	v_pk_add_f32 v[148:149], v[136:137], v[148:149]
	global_store_dwordx4 v4, v[146:149], s[100:101] offset:64
	global_load_dwordx4 v[134:137], v4, s[4:5] offset:64
	s_waitcnt vmcnt(17)
	v_pk_add_f32 v[150:151], v[130:131], v[150:151]
	v_pk_add_f32 v[152:153], v[132:133], v[152:153]
	global_store_dwordx4 v4, v[150:153], s[100:101] offset:512
	global_load_dwordx4 v[130:133], v4, s[4:5] offset:512
	s_waitcnt vmcnt(18)
	v_pk_add_f32 v[154:155], v[118:119], v[154:155]
	v_pk_add_f32 v[156:157], v[120:121], v[156:157]
	global_store_dwordx4 v4, v[154:157], s[100:101] offset:576
	global_load_dwordx4 v[118:121], v4, s[4:5] offset:576
	s_add_u32 s100, s12, 0x20000
	s_addc_u32 s101, s13, 0
	s_add_u32 s4, s56, 0x120000
	s_addc_u32 s5, s57, 0
	s_waitcnt vmcnt(19)
	v_pk_add_f32 v[158:159], v[126:127], v[158:159]
	v_pk_add_f32 v[160:161], v[128:129], v[160:161]
	global_store_dwordx4 v4, v[158:161], s[100:101]
	global_load_dwordx4 v[126:129], v4, s[4:5]
	s_waitcnt vmcnt(20)
	v_pk_add_f32 v[162:163], v[122:123], v[162:163]
	v_pk_add_f32 v[164:165], v[124:125], v[164:165]
	global_store_dwordx4 v4, v[162:165], s[100:101] offset:64
	global_load_dwordx4 v[122:125], v4, s[4:5] offset:64
	s_waitcnt vmcnt(21)
	v_pk_add_f32 v[166:167], v[114:115], v[166:167]
	v_pk_add_f32 v[168:169], v[116:117], v[168:169]
	global_store_dwordx4 v4, v[166:169], s[100:101] offset:512
	global_load_dwordx4 v[114:117], v4, s[4:5] offset:512
	s_waitcnt vmcnt(22)
	v_pk_add_f32 v[170:171], v[102:103], v[170:171]
	v_pk_add_f32 v[172:173], v[104:105], v[172:173]
	global_store_dwordx4 v4, v[170:173], s[100:101] offset:576
	global_load_dwordx4 v[102:105], v4, s[4:5] offset:576
	s_add_u32 s100, s12, 0x40000
	s_addc_u32 s101, s13, 0
	s_add_u32 s4, s56, 0x140000
	s_addc_u32 s5, s57, 0
	s_waitcnt vmcnt(23)
	v_pk_add_f32 v[174:175], v[110:111], v[174:175]
	v_pk_add_f32 v[176:177], v[112:113], v[176:177]
	global_store_dwordx4 v4, v[174:177], s[100:101]
	global_load_dwordx4 v[110:113], v4, s[4:5]
	s_waitcnt vmcnt(24)
;     __device__ __forceinline__ void operator()(const f32x4 (&acc)[2][2][4][2], const Unit& u, int wr, int wc, int fr, int fq) const {
;     ...
;             for (int m = 0; m < 4; ++m) { const size_t off = (size_t)(row0 + ai * HALF + m * 16) * ldc + col0;
; #pragma unroll
;                 for (int bj = 0; bj < 2; ++bj)
; #pragma unroll
;                     for (int n = 0; n < 2; ++n) { const f32x4 b = *(const f32x4*)(base + off + bj * HALF + n * 16); *(f32x4*)(out + off + bj * HALF + n * 16) = acc[ai][bj][m][n] + b; } }
	v_pk_add_f32 v[178:179], v[106:107], v[178:179]
	v_pk_add_f32 v[180:181], v[108:109], v[180:181]
	global_store_dwordx4 v4, v[178:181], s[100:101] offset:64
	global_load_dwordx4 v[106:109], v4, s[4:5] offset:64
	s_waitcnt vmcnt(25)
	v_pk_add_f32 v[182:183], v[98:99], v[182:183]
	v_pk_add_f32 v[184:185], v[100:101], v[184:185]
	global_store_dwordx4 v4, v[182:185], s[100:101] offset:512
	global_load_dwordx4 v[98:101], v4, s[4:5] offset:512
	s_waitcnt vmcnt(26)
	v_pk_add_f32 v[186:187], v[86:87], v[186:187]
	v_pk_add_f32 v[188:189], v[88:89], v[188:189]
	global_store_dwordx4 v4, v[186:189], s[100:101] offset:576
	global_load_dwordx4 v[86:89], v4, s[4:5] offset:576
	s_add_u32 s100, s12, 0x60000
	s_addc_u32 s101, s13, 0
	s_add_u32 s4, s56, 0x160000
	s_addc_u32 s5, s57, 0
	s_waitcnt vmcnt(27)
	v_pk_add_f32 v[190:191], v[94:95], v[190:191]
	v_pk_add_f32 v[192:193], v[96:97], v[192:193]
	global_store_dwordx4 v4, v[190:193], s[100:101]
	global_load_dwordx4 v[94:97], v4, s[4:5]
	s_waitcnt vmcnt(28)
	v_pk_add_f32 v[194:195], v[90:91], v[194:195]
	v_pk_add_f32 v[196:197], v[92:93], v[196:197]
	global_store_dwordx4 v4, v[194:197], s[100:101] offset:64
	global_load_dwordx4 v[90:93], v4, s[4:5] offset:64
	s_waitcnt vmcnt(29)
	v_pk_add_f32 v[198:199], v[82:83], v[198:199]
	v_pk_add_f32 v[200:201], v[84:85], v[200:201]
	global_store_dwordx4 v4, v[198:201], s[100:101] offset:512
	global_load_dwordx4 v[82:85], v4, s[4:5] offset:512
	s_waitcnt vmcnt(30)
	v_pk_add_f32 v[202:203], v[78:79], v[202:203]
	v_pk_add_f32 v[204:205], v[80:81], v[204:205]
	global_store_dwordx4 v4, v[202:205], s[100:101] offset:576
	global_load_dwordx4 v[78:81], v4, s[4:5] offset:576
	s_add_u32 s100, s12, 0x100000
	s_addc_u32 s101, s13, 0
	s_waitcnt vmcnt(30)
	v_pk_add_f32 v[138:139], v[74:75], v[138:139]
	v_pk_add_f32 v[140:141], v[76:77], v[140:141]
	global_store_dwordx4 v4, v[138:141], s[100:101]
	s_waitcnt vmcnt(29)
	v_pk_add_f32 v[134:135], v[70:71], v[134:135]
	v_pk_add_f32 v[136:137], v[72:73], v[136:137]
	global_store_dwordx4 v4, v[134:137], s[100:101] offset:64
	s_waitcnt vmcnt(28)
	v_pk_add_f32 v[130:131], v[66:67], v[130:131]
	v_pk_add_f32 v[132:133], v[68:69], v[132:133]
	global_store_dwordx4 v4, v[130:133], s[100:101] offset:512
	s_waitcnt vmcnt(27)
	v_pk_add_f32 v[118:119], v[54:55], v[118:119]
	v_pk_add_f32 v[120:121], v[56:57], v[120:121]
	global_store_dwordx4 v4, v[118:121], s[100:101] offset:576
	s_add_u32 s100, s12, 0x120000
	s_addc_u32 s101, s13, 0
	s_waitcnt vmcnt(26)
	v_pk_add_f32 v[126:127], v[62:63], v[126:127]
	v_pk_add_f32 v[128:129], v[64:65], v[128:129]
	global_store_dwordx4 v4, v[126:129], s[100:101]
	s_waitcnt vmcnt(25)
	v_pk_add_f32 v[122:123], v[58:59], v[122:123]
	v_pk_add_f32 v[124:125], v[60:61], v[124:125]
	global_store_dwordx4 v4, v[122:125], s[100:101] offset:64
	s_waitcnt vmcnt(24)
	v_pk_add_f32 v[114:115], v[50:51], v[114:115]
	v_pk_add_f32 v[116:117], v[52:53], v[116:117]
	global_store_dwordx4 v4, v[114:117], s[100:101] offset:512
	s_waitcnt vmcnt(23)
	v_pk_add_f32 v[102:103], v[38:39], v[102:103]
	v_pk_add_f32 v[104:105], v[40:41], v[104:105]
	global_store_dwordx4 v4, v[102:105], s[100:101] offset:576
	s_add_u32 s100, s12, 0x140000
	s_addc_u32 s101, s13, 0
	s_waitcnt vmcnt(22)
	v_pk_add_f32 v[110:111], v[46:47], v[110:111]
	v_pk_add_f32 v[112:113], v[48:49], v[112:113]
	global_store_dwordx4 v4, v[110:113], s[100:101]
	s_waitcnt vmcnt(21)
	v_pk_add_f32 v[106:107], v[42:43], v[106:107]
	v_pk_add_f32 v[108:109], v[44:45], v[108:109]
	global_store_dwordx4 v4, v[106:109], s[100:101] offset:64
	s_waitcnt vmcnt(20)
	v_pk_add_f32 v[98:99], v[34:35], v[98:99]
	v_pk_add_f32 v[100:101], v[36:37], v[100:101]
	global_store_dwordx4 v4, v[98:101], s[100:101] offset:512
	s_waitcnt vmcnt(19)
	v_pk_add_f32 v[86:87], v[22:23], v[86:87]
	v_pk_add_f32 v[88:89], v[24:25], v[88:89]
	global_store_dwordx4 v4, v[86:89], s[100:101] offset:576
	s_add_u32 s100, s12, 0x160000
	s_addc_u32 s101, s13, 0
	s_waitcnt vmcnt(18)
	v_pk_add_f32 v[94:95], v[30:31], v[94:95]
	v_pk_add_f32 v[96:97], v[32:33], v[96:97]
	global_store_dwordx4 v4, v[94:97], s[100:101]
	s_waitcnt vmcnt(17)
	v_pk_add_f32 v[90:91], v[26:27], v[90:91]
	v_pk_add_f32 v[92:93], v[28:29], v[92:93]
	global_store_dwordx4 v4, v[90:93], s[100:101] offset:64
	s_waitcnt vmcnt(16)
	v_pk_add_f32 v[82:83], v[18:19], v[82:83]
	v_pk_add_f32 v[84:85], v[20:21], v[84:85]
	global_store_dwordx4 v4, v[82:85], s[100:101] offset:512
	s_waitcnt vmcnt(15)
	v_pk_add_f32 v[78:79], v[14:15], v[78:79]
	v_pk_add_f32 v[80:81], v[16:17], v[80:81]
	global_store_dwordx4 v4, v[78:81], s[100:101] offset:576
	s_cbranch_vccnz .LBB0_550
	s_mov_b32 s20, s10
	s_mov_b32 s55, s14
	s_mov_b64 s[4:5], s[18:19]
	s_mov_b64 s[24:25], s[16:17]
	s_branch .LBB0_528

.LBB0_780:
	s_ashr_i32 s23, s22, 31
	s_lshl_b64 s[2:3], s[22:23], 19
	s_add_u32 s28, s0, s2
	s_addc_u32 s29, s1, s3
	s_and_b64 s[2:3], s[20:21], exec
	v_readlane_b32 s2, v251, 49
	s_cselect_b32 s23, s29, s45
	s_cselect_b32 s25, s28, s44
	s_add_u32 s30, s2, s26
	v_readlane_b32 s2, v251, 31
	s_addc_u32 s31, s2, s27
	s_and_b64 s[2:3], s[20:21], exec
	s_cselect_b32 s35, s31, s43
	s_cselect_b32 s61, s30, s42
	s_cmpk_gt_i32 s40, 0x80
	s_cselect_b64 s[40:41], -1, 0
	s_add_u32 s62, s42, 0x108000
	s_addc_u32 s63, s43, 0
	v_mov_b32_e32 v68, v67
	v_mov_b32_e32 v69, v67
	s_add_u32 s42, s44, 0x40080
	v_mov_b32_e32 v66, v67
	v_mov_b32_e32 v142, 0
	v_mov_b64_e32 v[80:81], v[68:69]
	v_mov_b64_e32 v[84:85], v[68:69]
	v_mov_b64_e32 v[96:97], v[68:69]
	v_mov_b64_e32 v[100:101], v[68:69]
	v_mov_b64_e32 v[112:113], v[68:69]
	v_mov_b64_e32 v[116:117], v[68:69]
	v_mov_b64_e32 v[128:129], v[68:69]
	v_mov_b64_e32 v[132:133], v[68:69]
	v_mov_b64_e32 v[88:89], v[68:69]
	v_mov_b64_e32 v[92:93], v[68:69]
	v_mov_b64_e32 v[104:105], v[68:69]
	v_mov_b64_e32 v[108:109], v[68:69]
	v_mov_b64_e32 v[120:121], v[68:69]
	v_mov_b64_e32 v[124:125], v[68:69]
	v_mov_b64_e32 v[136:137], v[68:69]
	v_mov_b64_e32 v[140:141], v[68:69]
	s_addc_u32 s43, s45, 0
	s_mov_b32 s64, -2
	v_mov_b64_e32 v[78:79], v[66:67]
	v_mov_b64_e32 v[82:83], v[66:67]
	v_mov_b64_e32 v[94:95], v[66:67]
	v_mov_b64_e32 v[98:99], v[66:67]
	v_mov_b64_e32 v[110:111], v[66:67]
	v_mov_b64_e32 v[114:115], v[66:67]
	v_mov_b64_e32 v[126:127], v[66:67]
	v_mov_b64_e32 v[130:131], v[66:67]
	v_mov_b64_e32 v[86:87], v[66:67]
	v_mov_b64_e32 v[90:91], v[66:67]
	v_mov_b64_e32 v[102:103], v[66:67]
	v_mov_b64_e32 v[106:107], v[66:67]
	v_mov_b64_e32 v[118:119], v[66:67]
	v_mov_b64_e32 v[122:123], v[66:67]
	v_mov_b64_e32 v[134:135], v[66:67]
	v_mov_b64_e32 v[138:139], v[66:67]
	v_mov_b32_e32 v143, v142
	v_mov_b32_e32 v144, v142
	v_mov_b32_e32 v145, v142
	v_mov_b32_e32 v146, v142
	v_mov_b32_e32 v147, v142
	v_mov_b32_e32 v148, v142
	v_mov_b32_e32 v149, v142
	v_mov_b32_e32 v158, v142
	v_mov_b32_e32 v159, v142
	v_mov_b32_e32 v160, v142
	v_mov_b32_e32 v161, v142
	v_mov_b32_e32 v162, v142
	v_mov_b32_e32 v163, v142
	v_mov_b32_e32 v164, v142
	v_mov_b32_e32 v165, v142
	v_mov_b32_e32 v174, v142
	v_mov_b32_e32 v175, v142
	v_mov_b32_e32 v176, v142
	v_mov_b32_e32 v177, v142
	v_mov_b32_e32 v178, v142
	v_mov_b32_e32 v179, v142
	v_mov_b32_e32 v180, v142
	v_mov_b32_e32 v181, v142
	v_mov_b32_e32 v190, v142
	v_mov_b32_e32 v191, v142
	v_mov_b32_e32 v192, v142
	v_mov_b32_e32 v193, v142
	v_mov_b32_e32 v194, v142
	v_mov_b32_e32 v195, v142
	v_mov_b32_e32 v196, v142
	v_mov_b32_e32 v197, v142
	v_mov_b32_e32 v150, v142
	v_mov_b32_e32 v151, v142
	v_mov_b32_e32 v152, v142
	v_mov_b32_e32 v153, v142
	v_mov_b32_e32 v154, v142
	v_mov_b32_e32 v155, v142
	v_mov_b32_e32 v156, v142
	v_mov_b32_e32 v157, v142
	v_mov_b32_e32 v166, v142
	v_mov_b32_e32 v167, v142
	v_mov_b32_e32 v168, v142
	v_mov_b32_e32 v169, v142
	v_mov_b32_e32 v170, v142
	v_mov_b32_e32 v171, v142
	v_mov_b32_e32 v172, v142
	v_mov_b32_e32 v173, v142
	v_mov_b32_e32 v182, v142
	v_mov_b32_e32 v183, v142
	v_mov_b32_e32 v184, v142
	v_mov_b32_e32 v185, v142
	v_mov_b32_e32 v186, v142
	v_mov_b32_e32 v187, v142
	v_mov_b32_e32 v188, v142
	v_mov_b32_e32 v189, v142
	v_mov_b32_e32 v198, v142
	v_mov_b32_e32 v199, v142
	v_mov_b32_e32 v200, v142
	v_mov_b32_e32 v201, v142
	v_mov_b32_e32 v202, v142
	v_mov_b32_e32 v203, v142
	v_mov_b32_e32 v204, v142
	v_mov_b32_e32 v205, v142
	s_waitcnt vmcnt(0)
	v_readfirstlane_b32 s101, v0
	s_nop 3
	s_and_b32 s101, s101, 0x3ff
	s_lshr_b32 s101, s101, 6
	s_cmp_ge_u32 s101, 4
	s_cbranch_scc0 .Lprio_p7_done
	s_setprio 1
.Lprio_p7_done:
	s_branch .LBB0_782
.LBB0_781:
	s_barrier
	s_add_i32 s64, s64, 2
	s_add_u32 s62, s62, 0x108000
	s_addc_u32 s63, s63, 0
	s_add_u32 s42, s42, 0x100
	s_addc_u32 s43, s43, 0
	s_cmp_gt_u32 s64, 13
	s_cbranch_scc1 .LBB0_798

;     __device__ __forceinline__ void finish(v4i_t& t0, v4i_t& t1, int j, int tid) const {
;         asm volatile("" : "+v"(t0), "+v"(t1));
;         const float* s0; unsigned char* d; addr(j, tid, s0, d);
;         const f32x4 r0 = __builtin_bit_cast(f32x4, t0) * 64.f, r1 = __builtin_bit_cast(f32x4, t1) * 64.f;
;         int w0 = 0, w1 = 0; w0 = __builtin_amdgcn_cvt_pk_fp8_f32(r0[0], r1[0], w0, false); w0 = __builtin_amdgcn_cvt_pk_fp8_f32(r0[1], r1[1], w0, true);
;         w1 = __builtin_amdgcn_cvt_pk_fp8_f32(r0[2], r1[2], w1, false); w1 = __builtin_amdgcn_cvt_pk_fp8_f32(r0[3], r1[3], w1, true);
;         typedef int v2is __attribute__((ext_vector_type(2))); __builtin_nontemporal_store((v2is){w0, w1}, (v2is*)d);
.Lp7vg_wd_a1:
	s_waitcnt lgkmcnt(0)
	s_barrier
	s_cmp_lt_i32 s98, 0
	s_cbranch_scc1 .Lp7vg_mmslow_a
	s_cmpk_gt_i32 s48, 0x7f
	s_cbranch_scc1 .Lp7vg_mmslow_a
	s_waitcnt lgkmcnt(0)
	v_mfma_scale_f32_16x16x128_f8f6f4 v[202:205], v[26:33], v[58:65], v[202:205], v226, v226 op_sel_hi:[0,0,0]
	s_add_i32 s4, s98, s52
	s_add_i32 s4, s4, 1
	v_pk_mul_f32 v[70:71], v[70:71], s[14:15] op_sel_hi:[1,0]
	v_pk_mul_f32 v[72:73], v[72:73], s[14:15] op_sel_hi:[1,0]
	v_mfma_scale_f32_16x16x128_f8f6f4 v[198:201], v[18:25], v[58:65], v[198:201], v226, v226 op_sel_hi:[0,0,0]
	v_pk_mul_f32 v[74:75], v[74:75], s[14:15] op_sel_hi:[1,0]
	v_pk_mul_f32 v[76:77], v[76:77], s[14:15] op_sel_hi:[1,0]
	s_ashr_i32 s2, s4, 10
	s_ashr_i32 s3, s2, 31
	v_mfma_scale_f32_16x16x128_f8f6f4 v[186:189], v[26:33], v[50:57], v[186:189], v226, v226 op_sel_hi:[0,0,0]
	v_cvt_pk_fp8_f32 v70, v70, v74
	s_lshl_b32 s4, s4, 12
	s_lshl_b64 s[2:3], s[2:3], 22
	v_cvt_pk_fp8_f32 v70, v71, v75 op_sel:[0,0,1]
	v_mfma_scale_f32_16x16x128_f8f6f4 v[182:185], v[18:25], v[50:57], v[182:185], v226, v226 op_sel_hi:[0,0,0]
	s_and_b32 s4, s4, 0x3ff000
	v_readlane_b32 s5, v251, 50
	v_cvt_pk_fp8_f32 v71, v72, v76
	s_add_u32 s2, s5, s2
	v_mfma_scale_f32_16x16x128_f8f6f4 v[170:173], v[26:33], v[42:49], v[170:173], v226, v226 op_sel_hi:[0,0,0]
	v_readlane_b32 s5, v251, 51
	s_addc_u32 s3, s5, s3
	v_cvt_pk_fp8_f32 v71, v73, v77 op_sel:[0,0,1]
	s_add_u32 s2, s2, s4
	s_addc_u32 s3, s3, 0
	v_mfma_scale_f32_16x16x128_f8f6f4 v[166:169], v[18:25], v[42:49], v[166:169], v226, v226 op_sel_hi:[0,0,0]
	v_lshl_add_u64 v[68:69], s[2:3], 0, v[210:211]
	global_store_dwordx2 v[68:69], v[70:71], off nt
	s_add_i32 s4, s48, s53
	s_ashr_i32 s2, s4, 10
	v_mfma_scale_f32_16x16x128_f8f6f4 v[154:157], v[26:33], v[34:41], v[154:157], v226, v226 op_sel_hi:[0,0,0]
	s_ashr_i32 s3, s2, 31
	s_lshl_b64 s[2:3], s[2:3], 24
	s_lshl_b32 s4, s4, 14
	s_and_b32 s4, s4, 0xffc000
	v_mfma_scale_f32_16x16x128_f8f6f4 v[150:153], v[18:25], v[34:41], v[150:153], v226, v226 op_sel_hi:[0,0,0]
	s_add_u32 s2, s76, s2
	s_addc_u32 s3, s77, s3
	s_add_u32 s2, s2, s4
	s_addc_u32 s3, s3, 0
	v_mfma_scale_f32_16x16x128_f8f6f4 v[194:197], v[10:17], v[58:65], v[194:197], v226, v226 op_sel_hi:[0,0,0]
	v_lshlrev_b32_e32 v66, 2, v208
	v_lshl_add_u64 v[68:69], s[2:3], 0, v[66:67]
	v_lshl_add_u64 v[68:69], v[68:69], 0, s[16:17]
	global_load_dwordx4 v[70:73], v66, s[2:3] nt
	v_mfma_scale_f32_16x16x128_f8f6f4 v[190:193], v[2:9], v[58:65], v[190:193], v226, v226 op_sel_hi:[0,0,0]
	global_load_dwordx4 v[74:77], v[68:69], off nt
	s_mov_b32 s100, 3
	s_mov_b32 s98, s48
	s_add_i32 s48, s48, 1
	v_mfma_scale_f32_16x16x128_f8f6f4 v[178:181], v[10:17], v[50:57], v[178:181], v226, v226 op_sel_hi:[0,0,0]
	s_add_u32 s2, s42, 0xfffc0080
	s_addc_u32 s3, s43, -1
	s_cmp_eq_u32 s64, 12
	s_cselect_b32 s5, s23, s3
	s_cselect_b32 s4, s25, s2
	s_cselect_b32 s45, s35, s63
	s_cselect_b32 s44, s61, s62
	v_mfma_scale_f32_16x16x128_f8f6f4 v[174:177], v[2:9], v[50:57], v[174:177], v226, v226 op_sel_hi:[0,0,0]
	v_mfma_scale_f32_16x16x128_f8f6f4 v[162:165], v[10:17], v[42:49], v[162:165], v226, v226 op_sel_hi:[0,0,0]
	v_mfma_scale_f32_16x16x128_f8f6f4 v[158:161], v[2:9], v[42:49], v[158:161], v226, v226 op_sel_hi:[0,0,0]
	v_mfma_scale_f32_16x16x128_f8f6f4 v[146:149], v[10:17], v[34:41], v[146:149], v226, v226 op_sel_hi:[0,0,0]
	v_mfma_scale_f32_16x16x128_f8f6f4 v[142:145], v[2:9], v[34:41], v[142:145], v226, v226 op_sel_hi:[0,0,0]
	s_branch .Lp7vg_mmjoin_a

.Lp7vg_ni_a:
	s_add_u32 s2, s42, 0xfffc0080
	s_addc_u32 s3, s43, -1
	s_cmp_eq_u32 s64, 12
	s_cselect_b32 s5, s23, s3
	s_cselect_b32 s4, s25, s2
	s_cselect_b32 s45, s35, s63
	s_cselect_b32 s44, s61, s62
	s_waitcnt lgkmcnt(0)
	v_mfma_scale_f32_16x16x128_f8f6f4 v[202:205], v[26:33], v[58:65], v[202:205], v226, v226 op_sel_hi:[0,0,0]
	v_mfma_scale_f32_16x16x128_f8f6f4 v[198:201], v[18:25], v[58:65], v[198:201], v226, v226 op_sel_hi:[0,0,0]
	v_mfma_scale_f32_16x16x128_f8f6f4 v[186:189], v[26:33], v[50:57], v[186:189], v226, v226 op_sel_hi:[0,0,0]
	v_mfma_scale_f32_16x16x128_f8f6f4 v[182:185], v[18:25], v[50:57], v[182:185], v226, v226 op_sel_hi:[0,0,0]
	v_mfma_scale_f32_16x16x128_f8f6f4 v[170:173], v[26:33], v[42:49], v[170:173], v226, v226 op_sel_hi:[0,0,0]
	v_mfma_scale_f32_16x16x128_f8f6f4 v[166:169], v[18:25], v[42:49], v[166:169], v226, v226 op_sel_hi:[0,0,0]
	v_mfma_scale_f32_16x16x128_f8f6f4 v[154:157], v[26:33], v[34:41], v[154:157], v226, v226 op_sel_hi:[0,0,0]
	v_mfma_scale_f32_16x16x128_f8f6f4 v[150:153], v[18:25], v[34:41], v[150:153], v226, v226 op_sel_hi:[0,0,0]
	v_mfma_scale_f32_16x16x128_f8f6f4 v[194:197], v[10:17], v[58:65], v[194:197], v226, v226 op_sel_hi:[0,0,0]
	v_mfma_scale_f32_16x16x128_f8f6f4 v[190:193], v[2:9], v[58:65], v[190:193], v226, v226 op_sel_hi:[0,0,0]
	v_mfma_scale_f32_16x16x128_f8f6f4 v[178:181], v[10:17], v[50:57], v[178:181], v226, v226 op_sel_hi:[0,0,0]
	v_mfma_scale_f32_16x16x128_f8f6f4 v[174:177], v[2:9], v[50:57], v[174:177], v226, v226 op_sel_hi:[0,0,0]
	v_mfma_scale_f32_16x16x128_f8f6f4 v[162:165], v[10:17], v[42:49], v[162:165], v226, v226 op_sel_hi:[0,0,0]
	v_mfma_scale_f32_16x16x128_f8f6f4 v[158:161], v[2:9], v[42:49], v[158:161], v226, v226 op_sel_hi:[0,0,0]
	v_mfma_scale_f32_16x16x128_f8f6f4 v[146:149], v[10:17], v[34:41], v[146:149], v226, v226 op_sel_hi:[0,0,0]
	v_mfma_scale_f32_16x16x128_f8f6f4 v[142:145], v[2:9], v[34:41], v[142:145], v226, v226 op_sel_hi:[0,0,0]

.Lp7dma_wd_a:
	s_waitcnt lgkmcnt(0)
	s_barrier
	s_cbranch_vccnz .Lp7dma_skip_b
	s_waitcnt lgkmcnt(0)
	v_mfma_scale_f32_16x16x128_f8f6f4 v[138:141], v[26:33], v[58:65], v[138:141], v226, v226 op_sel_hi:[0,0,0]
	v_mfma_scale_f32_16x16x128_f8f6f4 v[134:137], v[18:25], v[58:65], v[134:137], v226, v226 op_sel_hi:[0,0,0]
	v_mfma_scale_f32_16x16x128_f8f6f4 v[122:125], v[26:33], v[50:57], v[122:125], v226, v226 op_sel_hi:[0,0,0]
	v_mfma_scale_f32_16x16x128_f8f6f4 v[118:121], v[18:25], v[50:57], v[118:121], v226, v226 op_sel_hi:[0,0,0]
	v_mfma_scale_f32_16x16x128_f8f6f4 v[106:109], v[26:33], v[42:49], v[106:109], v226, v226 op_sel_hi:[0,0,0]
	v_mfma_scale_f32_16x16x128_f8f6f4 v[102:105], v[18:25], v[42:49], v[102:105], v226, v226 op_sel_hi:[0,0,0]
	v_mfma_scale_f32_16x16x128_f8f6f4 v[90:93], v[26:33], v[34:41], v[90:93], v226, v226 op_sel_hi:[0,0,0]
	v_mfma_scale_f32_16x16x128_f8f6f4 v[86:89], v[18:25], v[34:41], v[86:89], v226, v226 op_sel_hi:[0,0,0]
	v_mfma_scale_f32_16x16x128_f8f6f4 v[130:133], v[10:17], v[58:65], v[130:133], v226, v226 op_sel_hi:[0,0,0]
	v_mfma_scale_f32_16x16x128_f8f6f4 v[126:129], v[2:9], v[58:65], v[126:129], v226, v226 op_sel_hi:[0,0,0]
	v_mfma_scale_f32_16x16x128_f8f6f4 v[114:117], v[10:17], v[50:57], v[114:117], v226, v226 op_sel_hi:[0,0,0]
	v_lshl_add_u64 v[68:69], s[4:5], 0, v[212:213]
	s_mov_b32 m0, s15
	v_cmp_ne_u32_e64 s[2:3], 1, v66
	global_load_lds_dwordx4 v[68:69], off
	v_mfma_scale_f32_16x16x128_f8f6f4 v[110:113], v[2:9], v[50:57], v[110:113], v226, v226 op_sel_hi:[0,0,0]
	v_mfma_scale_f32_16x16x128_f8f6f4 v[98:101], v[10:17], v[42:49], v[98:101], v226, v226 op_sel_hi:[0,0,0]
	s_mov_b32 m0, s49
	s_nop 0
	global_load_lds_dwordx4 v[224:225], off
	v_mfma_scale_f32_16x16x128_f8f6f4 v[94:97], v[2:9], v[42:49], v[94:97], v226, v226 op_sel_hi:[0,0,0]
	v_mfma_scale_f32_16x16x128_f8f6f4 v[82:85], v[10:17], v[34:41], v[82:85], v226, v226 op_sel_hi:[0,0,0]
	v_mfma_scale_f32_16x16x128_f8f6f4 v[78:81], v[2:9], v[34:41], v[78:81], v226, v226 op_sel_hi:[0,0,0]

;     __device__ __forceinline__ void finish(v4i_t& t0, v4i_t& t1, int j, int tid) const {
;         asm volatile("" : "+v"(t0), "+v"(t1));
;         const float* s0; unsigned char* d; addr(j, tid, s0, d);
;         const f32x4 r0 = __builtin_bit_cast(f32x4, t0) * 64.f, r1 = __builtin_bit_cast(f32x4, t1) * 64.f;
;         int w0 = 0, w1 = 0; w0 = __builtin_amdgcn_cvt_pk_fp8_f32(r0[0], r1[0], w0, false); w0 = __builtin_amdgcn_cvt_pk_fp8_f32(r0[1], r1[1], w0, true);
;         w1 = __builtin_amdgcn_cvt_pk_fp8_f32(r0[2], r1[2], w1, false); w1 = __builtin_amdgcn_cvt_pk_fp8_f32(r0[3], r1[3], w1, true);
;         typedef int v2is __attribute__((ext_vector_type(2))); __builtin_nontemporal_store((v2is){w0, w1}, (v2is*)d);
.Lp7vg_wd_b1:
	s_waitcnt lgkmcnt(0)
	s_barrier
	s_cmp_lt_i32 s99, 0
	s_cbranch_scc1 .Lp7vg_mmslow_b
	s_cmpk_gt_i32 s48, 0x7f
	s_cbranch_scc1 .Lp7vg_mmslow_b
	s_waitcnt lgkmcnt(0)
	v_mfma_scale_f32_16x16x128_f8f6f4 v[202:205], v[26:33], v[58:65], v[202:205], v226, v226 op_sel_hi:[0,0,0]
	s_add_i32 s65, s99, s52
	s_add_i32 s65, s65, 1
	v_pk_mul_f32 v[242:243], v[242:243], s[14:15] op_sel_hi:[1,0]
	v_pk_mul_f32 v[244:245], v[244:245], s[14:15] op_sel_hi:[1,0]
	v_mfma_scale_f32_16x16x128_f8f6f4 v[198:201], v[18:25], v[58:65], v[198:201], v226, v226 op_sel_hi:[0,0,0]
	v_pk_mul_f32 v[246:247], v[246:247], s[14:15] op_sel_hi:[1,0]
	v_pk_mul_f32 v[248:249], v[248:249], s[14:15] op_sel_hi:[1,0]
	s_ashr_i32 s46, s65, 10
	s_ashr_i32 s47, s46, 31
	v_mfma_scale_f32_16x16x128_f8f6f4 v[186:189], v[26:33], v[50:57], v[186:189], v226, v226 op_sel_hi:[0,0,0]
	v_cvt_pk_fp8_f32 v242, v242, v246
	s_lshl_b32 s65, s65, 12
	s_lshl_b64 s[46:47], s[46:47], 22
	v_cvt_pk_fp8_f32 v242, v243, v247 op_sel:[0,0,1]
	v_mfma_scale_f32_16x16x128_f8f6f4 v[182:185], v[18:25], v[50:57], v[182:185], v226, v226 op_sel_hi:[0,0,0]
	s_and_b32 s65, s65, 0x3ff000
	v_readlane_b32 s4, v251, 50
	v_cvt_pk_fp8_f32 v243, v244, v248
	s_add_u32 s46, s4, s46
	v_mfma_scale_f32_16x16x128_f8f6f4 v[170:173], v[26:33], v[42:49], v[170:173], v226, v226 op_sel_hi:[0,0,0]
	v_readlane_b32 s4, v251, 51
	s_addc_u32 s47, s4, s47
	v_cvt_pk_fp8_f32 v243, v245, v249 op_sel:[0,0,1]
	s_add_u32 s46, s46, s65
	s_addc_u32 s47, s47, 0
	v_mfma_scale_f32_16x16x128_f8f6f4 v[166:169], v[18:25], v[42:49], v[166:169], v226, v226 op_sel_hi:[0,0,0]
	v_lshl_add_u64 v[240:241], s[46:47], 0, v[210:211]
	global_store_dwordx2 v[240:241], v[242:243], off nt
	s_add_i32 s65, s48, s53
	s_ashr_i32 s46, s65, 10
	v_mfma_scale_f32_16x16x128_f8f6f4 v[154:157], v[26:33], v[34:41], v[154:157], v226, v226 op_sel_hi:[0,0,0]
	s_ashr_i32 s47, s46, 31
	s_lshl_b64 s[46:47], s[46:47], 24
	s_lshl_b32 s65, s65, 14
	s_and_b32 s65, s65, 0xffc000
	v_mfma_scale_f32_16x16x128_f8f6f4 v[150:153], v[18:25], v[34:41], v[150:153], v226, v226 op_sel_hi:[0,0,0]
	s_add_u32 s46, s76, s46
	s_addc_u32 s47, s77, s47
	s_add_u32 s46, s46, s65
	s_addc_u32 s47, s47, 0
	v_mfma_scale_f32_16x16x128_f8f6f4 v[194:197], v[10:17], v[58:65], v[194:197], v226, v226 op_sel_hi:[0,0,0]
	v_lshlrev_b32_e32 v66, 2, v208
	v_lshl_add_u64 v[240:241], s[46:47], 0, v[66:67]
	v_lshl_add_u64 v[240:241], v[240:241], 0, s[16:17]
	global_load_dwordx4 v[242:245], v66, s[46:47] nt
	v_mfma_scale_f32_16x16x128_f8f6f4 v[190:193], v[2:9], v[58:65], v[190:193], v226, v226 op_sel_hi:[0,0,0]
	global_load_dwordx4 v[246:249], v[240:241], off nt
	s_mov_b32 s100, 3
	s_mov_b32 s99, s48
	s_add_i32 s48, s48, 1
	v_mfma_scale_f32_16x16x128_f8f6f4 v[178:181], v[10:17], v[50:57], v[178:181], v226, v226 op_sel_hi:[0,0,0]
	s_add_u32 s46, s44, 0x84000
	s_addc_u32 s47, s45, 0
	v_mfma_scale_f32_16x16x128_f8f6f4 v[174:177], v[2:9], v[50:57], v[174:177], v226, v226 op_sel_hi:[0,0,0]
	v_mfma_scale_f32_16x16x128_f8f6f4 v[162:165], v[10:17], v[42:49], v[162:165], v226, v226 op_sel_hi:[0,0,0]
	v_mfma_scale_f32_16x16x128_f8f6f4 v[158:161], v[2:9], v[42:49], v[158:161], v226, v226 op_sel_hi:[0,0,0]
	v_mfma_scale_f32_16x16x128_f8f6f4 v[146:149], v[10:17], v[34:41], v[146:149], v226, v226 op_sel_hi:[0,0,0]
	v_mfma_scale_f32_16x16x128_f8f6f4 v[142:145], v[2:9], v[34:41], v[142:145], v226, v226 op_sel_hi:[0,0,0]
	s_branch .Lp7vg_mmjoin_b

.Lp7vg_ni_b:
	s_add_u32 s46, s44, 0x84000
	s_addc_u32 s47, s45, 0
	s_waitcnt lgkmcnt(0)
	v_mfma_scale_f32_16x16x128_f8f6f4 v[202:205], v[26:33], v[58:65], v[202:205], v226, v226 op_sel_hi:[0,0,0]
	v_mfma_scale_f32_16x16x128_f8f6f4 v[198:201], v[18:25], v[58:65], v[198:201], v226, v226 op_sel_hi:[0,0,0]
	v_mfma_scale_f32_16x16x128_f8f6f4 v[186:189], v[26:33], v[50:57], v[186:189], v226, v226 op_sel_hi:[0,0,0]
	v_mfma_scale_f32_16x16x128_f8f6f4 v[182:185], v[18:25], v[50:57], v[182:185], v226, v226 op_sel_hi:[0,0,0]
	v_mfma_scale_f32_16x16x128_f8f6f4 v[170:173], v[26:33], v[42:49], v[170:173], v226, v226 op_sel_hi:[0,0,0]
	v_mfma_scale_f32_16x16x128_f8f6f4 v[166:169], v[18:25], v[42:49], v[166:169], v226, v226 op_sel_hi:[0,0,0]
	v_mfma_scale_f32_16x16x128_f8f6f4 v[154:157], v[26:33], v[34:41], v[154:157], v226, v226 op_sel_hi:[0,0,0]
	v_mfma_scale_f32_16x16x128_f8f6f4 v[150:153], v[18:25], v[34:41], v[150:153], v226, v226 op_sel_hi:[0,0,0]
	v_mfma_scale_f32_16x16x128_f8f6f4 v[194:197], v[10:17], v[58:65], v[194:197], v226, v226 op_sel_hi:[0,0,0]
	v_mfma_scale_f32_16x16x128_f8f6f4 v[190:193], v[2:9], v[58:65], v[190:193], v226, v226 op_sel_hi:[0,0,0]
	v_mfma_scale_f32_16x16x128_f8f6f4 v[178:181], v[10:17], v[50:57], v[178:181], v226, v226 op_sel_hi:[0,0,0]
	v_mfma_scale_f32_16x16x128_f8f6f4 v[174:177], v[2:9], v[50:57], v[174:177], v226, v226 op_sel_hi:[0,0,0]
	v_mfma_scale_f32_16x16x128_f8f6f4 v[162:165], v[10:17], v[42:49], v[162:165], v226, v226 op_sel_hi:[0,0,0]
	v_mfma_scale_f32_16x16x128_f8f6f4 v[158:161], v[2:9], v[42:49], v[158:161], v226, v226 op_sel_hi:[0,0,0]
	v_mfma_scale_f32_16x16x128_f8f6f4 v[146:149], v[10:17], v[34:41], v[146:149], v226, v226 op_sel_hi:[0,0,0]
	v_mfma_scale_f32_16x16x128_f8f6f4 v[142:145], v[2:9], v[34:41], v[142:145], v226, v226 op_sel_hi:[0,0,0]

.Lp7dma_wd_b:
	s_waitcnt lgkmcnt(0)
	s_barrier
	s_cbranch_vccnz .Lp7dma_skip_d
	s_waitcnt lgkmcnt(0)
	v_mfma_scale_f32_16x16x128_f8f6f4 v[138:141], v[26:33], v[58:65], v[138:141], v226, v226 op_sel_hi:[0,0,0]
	v_mfma_scale_f32_16x16x128_f8f6f4 v[134:137], v[18:25], v[58:65], v[134:137], v226, v226 op_sel_hi:[0,0,0]
	v_mfma_scale_f32_16x16x128_f8f6f4 v[122:125], v[26:33], v[50:57], v[122:125], v226, v226 op_sel_hi:[0,0,0]
	v_mfma_scale_f32_16x16x128_f8f6f4 v[118:121], v[18:25], v[50:57], v[118:121], v226, v226 op_sel_hi:[0,0,0]
	v_mfma_scale_f32_16x16x128_f8f6f4 v[106:109], v[26:33], v[42:49], v[106:109], v226, v226 op_sel_hi:[0,0,0]
	v_mfma_scale_f32_16x16x128_f8f6f4 v[102:105], v[18:25], v[42:49], v[102:105], v226, v226 op_sel_hi:[0,0,0]
	v_mfma_scale_f32_16x16x128_f8f6f4 v[90:93], v[26:33], v[34:41], v[90:93], v226, v226 op_sel_hi:[0,0,0]
	v_mfma_scale_f32_16x16x128_f8f6f4 v[86:89], v[18:25], v[34:41], v[86:89], v226, v226 op_sel_hi:[0,0,0]
	v_mfma_scale_f32_16x16x128_f8f6f4 v[130:133], v[10:17], v[58:65], v[130:133], v226, v226 op_sel_hi:[0,0,0]
	v_mfma_scale_f32_16x16x128_f8f6f4 v[126:129], v[2:9], v[58:65], v[126:129], v226, v226 op_sel_hi:[0,0,0]
	v_mfma_scale_f32_16x16x128_f8f6f4 v[114:117], v[10:17], v[50:57], v[114:117], v226, v226 op_sel_hi:[0,0,0]
	s_mov_b32 m0, s54
	s_nop 0
	global_load_lds_dwordx4 v[68:69], off
	v_mfma_scale_f32_16x16x128_f8f6f4 v[110:113], v[2:9], v[50:57], v[110:113], v226, v226 op_sel_hi:[0,0,0]
	v_mfma_scale_f32_16x16x128_f8f6f4 v[98:101], v[10:17], v[42:49], v[98:101], v226, v226 op_sel_hi:[0,0,0]
	v_lshl_add_u64 v[68:69], v[224:225], 0, s[10:11]
	s_mov_b32 m0, s55
	s_nop 0
	global_load_lds_dwordx4 v[68:69], off
	v_mfma_scale_f32_16x16x128_f8f6f4 v[94:97], v[2:9], v[42:49], v[94:97], v226, v226 op_sel_hi:[0,0,0]
	v_mfma_scale_f32_16x16x128_f8f6f4 v[82:85], v[10:17], v[34:41], v[82:85], v226, v226 op_sel_hi:[0,0,0]
	v_mfma_scale_f32_16x16x128_f8f6f4 v[78:81], v[2:9], v[34:41], v[78:81], v226, v226 op_sel_hi:[0,0,0]
	s_branch .LBB0_781

.LBB0_798:
	s_setprio 0
	s_and_b64 vcc, exec, s[12:13]
	s_cbranch_vccz .LBB0_800
	s_barrier

.LBB0_899:
	s_ashr_i32 s31, s30, 31
	s_lshl_b64 s[2:3], s[30:31], 19
	s_add_u32 s38, s6, s2
	s_addc_u32 s39, s7, s3
	s_and_b64 s[2:3], s[26:27], exec
	v_readlane_b32 s2, v251, 50
	s_cselect_b32 s29, s39, s53
	s_cselect_b32 s31, s38, s52
	s_add_u32 s40, s2, s36
	v_readlane_b32 s2, v251, 51
	s_addc_u32 s41, s2, s37
	s_and_b64 s[2:3], s[26:27], exec
	s_cselect_b32 s35, s41, s51
	s_cselect_b32 s43, s40, s50
	s_cmpk_gt_i32 s48, 0x80
	s_cselect_b64 s[48:49], -1, 0
	s_add_u32 s70, s50, 0x80000
	s_addc_u32 s71, s51, 0
	v_mov_b32_e32 v68, v66
	v_mov_b32_e32 v69, v66
	s_add_u32 s50, s52, 0x40080
	v_mov_b32_e32 v67, v66
	v_mov_b32_e32 v134, 0
	v_mov_b64_e32 v[72:73], v[68:69]
	v_mov_b64_e32 v[76:77], v[68:69]
	v_mov_b64_e32 v[88:89], v[68:69]
	v_mov_b64_e32 v[92:93], v[68:69]
	v_mov_b64_e32 v[104:105], v[68:69]
	v_mov_b64_e32 v[108:109], v[68:69]
	v_mov_b64_e32 v[120:121], v[68:69]
	v_mov_b64_e32 v[124:125], v[68:69]
	v_mov_b64_e32 v[80:81], v[68:69]
	v_mov_b64_e32 v[84:85], v[68:69]
	v_mov_b64_e32 v[96:97], v[68:69]
	v_mov_b64_e32 v[100:101], v[68:69]
	v_mov_b64_e32 v[112:113], v[68:69]
	v_mov_b64_e32 v[116:117], v[68:69]
	v_mov_b64_e32 v[128:129], v[68:69]
	v_mov_b64_e32 v[132:133], v[68:69]
	s_addc_u32 s51, s53, 0
	s_mov_b32 s72, -2
	v_cndmask_b32_e64 v225, 0, 1, s[48:49]
	v_mov_b64_e32 v[70:71], v[66:67]
	v_mov_b64_e32 v[74:75], v[66:67]
	v_mov_b64_e32 v[86:87], v[66:67]
	v_mov_b64_e32 v[90:91], v[66:67]
	v_mov_b64_e32 v[102:103], v[66:67]
	v_mov_b64_e32 v[106:107], v[66:67]
	v_mov_b64_e32 v[118:119], v[66:67]
	v_mov_b64_e32 v[122:123], v[66:67]
	v_mov_b64_e32 v[78:79], v[66:67]
	v_mov_b64_e32 v[82:83], v[66:67]
	v_mov_b64_e32 v[94:95], v[66:67]
	v_mov_b64_e32 v[98:99], v[66:67]
	v_mov_b64_e32 v[110:111], v[66:67]
	v_mov_b64_e32 v[114:115], v[66:67]
	v_mov_b64_e32 v[126:127], v[66:67]
	v_mov_b64_e32 v[130:131], v[66:67]
	v_mov_b32_e32 v135, v134
	v_mov_b32_e32 v136, v134
	v_mov_b32_e32 v137, v134
	v_mov_b32_e32 v138, v134
	v_mov_b32_e32 v139, v134
	v_mov_b32_e32 v140, v134
	v_mov_b32_e32 v141, v134
	v_mov_b32_e32 v150, v134
	v_mov_b32_e32 v151, v134
	v_mov_b32_e32 v152, v134
	v_mov_b32_e32 v153, v134
	v_mov_b32_e32 v154, v134
	v_mov_b32_e32 v155, v134
	v_mov_b32_e32 v156, v134
	v_mov_b32_e32 v157, v134
	v_mov_b32_e32 v166, v134
	v_mov_b32_e32 v167, v134
	v_mov_b32_e32 v168, v134
	v_mov_b32_e32 v169, v134
	v_mov_b32_e32 v170, v134
	v_mov_b32_e32 v171, v134
	v_mov_b32_e32 v172, v134
	v_mov_b32_e32 v173, v134
	v_mov_b32_e32 v174, v134
	v_mov_b32_e32 v175, v134
	v_mov_b32_e32 v176, v134
	v_mov_b32_e32 v177, v134
	v_mov_b32_e32 v178, v134
	v_mov_b32_e32 v179, v134
	v_mov_b32_e32 v180, v134
	v_mov_b32_e32 v181, v134
	v_mov_b32_e32 v142, v134
	v_mov_b32_e32 v143, v134
	v_mov_b32_e32 v144, v134
	v_mov_b32_e32 v145, v134
	v_mov_b32_e32 v146, v134
	v_mov_b32_e32 v147, v134
	v_mov_b32_e32 v148, v134
	v_mov_b32_e32 v149, v134
	v_mov_b32_e32 v158, v134
	v_mov_b32_e32 v159, v134
	v_mov_b32_e32 v160, v134
	v_mov_b32_e32 v161, v134
	v_mov_b32_e32 v162, v134
	v_mov_b32_e32 v163, v134
	v_mov_b32_e32 v164, v134
	v_mov_b32_e32 v165, v134
	v_mov_b32_e32 v182, v134
	v_mov_b32_e32 v183, v134
	v_mov_b32_e32 v184, v134
	v_mov_b32_e32 v185, v134
	v_mov_b32_e32 v186, v134
	v_mov_b32_e32 v187, v134
	v_mov_b32_e32 v188, v134
	v_mov_b32_e32 v189, v134
	v_mov_b32_e32 v190, v134
	v_mov_b32_e32 v191, v134
	v_mov_b32_e32 v192, v134
	v_mov_b32_e32 v193, v134
	v_mov_b32_e32 v194, v134
	v_mov_b32_e32 v195, v134
	v_mov_b32_e32 v196, v134
	v_mov_b32_e32 v197, v134
	s_waitcnt vmcnt(0)
	v_readfirstlane_b32 s101, v0
	s_nop 3
	s_and_b32 s101, s101, 0x3ff
	s_lshr_b32 s101, s101, 6
	s_cmp_ge_u32 s101, 4
	s_cbranch_scc0 .Lprio_p8_done
	s_setprio 1
.Lprio_p8_done:
	s_branch .LBB0_901
.LBB0_900:
	s_barrier
	s_add_i32 s72, s72, 2
	s_add_u32 s70, s70, 0x80000
	s_addc_u32 s71, s71, 0
	s_add_u32 s50, s50, 0x100
	s_addc_u32 s51, s51, 0
	s_cmp_gt_u32 s72, 13
	s_cbranch_scc1 .LBB0_905
.LBB0_901:
	ds_read_b64_tr_b16 v[26:27], v207 offset:0
	ds_read_b64_tr_b16 v[28:29], v207 offset:1024
	ds_read_b64_tr_b16 v[30:31], v207 offset:8192
	ds_read_b64_tr_b16 v[32:33], v207 offset:9216
	ds_read_b64_tr_b16 v[18:19], v217 offset:0
	ds_read_b64_tr_b16 v[20:21], v217 offset:1024
	ds_read_b64_tr_b16 v[22:23], v217 offset:8192
	ds_read_b64_tr_b16 v[24:25], v217 offset:9216
	ds_read_b64_tr_b16 v[10:11], v214 offset:0
	ds_read_b64_tr_b16 v[12:13], v214 offset:1024
	ds_read_b64_tr_b16 v[14:15], v214 offset:8192
	ds_read_b64_tr_b16 v[16:17], v214 offset:9216
	ds_read_b64_tr_b16 v[2:3], v218 offset:0
	ds_read_b64_tr_b16 v[4:5], v218 offset:1024
	ds_read_b64_tr_b16 v[6:7], v218 offset:8192
	ds_read_b64_tr_b16 v[8:9], v218 offset:9216
	s_add_u32 s2, s50, 0xfffc0080
	s_addc_u32 s3, s51, -1
	s_cmp_eq_u32 s72, 12
	s_cselect_b32 s55, s29, s3
	s_cselect_b32 s54, s31, s2
	s_cselect_b32 s53, s35, s71
	s_cselect_b32 s52, s43, s70
	ds_read_b128 v[34:37], v223
	ds_read_b128 v[38:41], v223 offset:1024
	ds_read_b128 v[42:45], v223 offset:2048
	ds_read_b128 v[46:49], v223 offset:3072
	ds_read_b128 v[50:53], v223 offset:4096
	ds_read_b128 v[54:57], v223 offset:5120
	ds_read_b128 v[58:61], v223 offset:6144
	ds_read_b128 v[62:65], v223 offset:7168
	s_waitcnt vmcnt(6)
	s_waitcnt lgkmcnt(0)
	s_barrier
	s_waitcnt lgkmcnt(0)
	v_mfma_scale_f32_16x16x128_f8f6f4 v[194:197], v[26:33], v[34:41], v[194:197], v1, v1 op_sel_hi:[0,0,0]
	v_mfma_scale_f32_16x16x128_f8f6f4 v[190:193], v[18:25], v[34:41], v[190:193], v1, v1 op_sel_hi:[0,0,0]
	v_mfma_scale_f32_16x16x128_f8f6f4 v[186:189], v[26:33], v[42:49], v[186:189], v1, v1 op_sel_hi:[0,0,0]
	v_mfma_scale_f32_16x16x128_f8f6f4 v[182:185], v[18:25], v[42:49], v[182:185], v1, v1 op_sel_hi:[0,0,0]
	v_lshl_add_u64 v[68:69], s[50:51], 0, v[208:209]
	s_add_i32 m0, s17, 0xc000
	s_nop 0
	global_load_lds_dwordx4 v[68:69], off
	v_mfma_scale_f32_16x16x128_f8f6f4 v[162:165], v[26:33], v[50:57], v[162:165], v1, v1 op_sel_hi:[0,0,0]
	v_mfma_scale_f32_16x16x128_f8f6f4 v[158:161], v[18:25], v[50:57], v[158:161], v1, v1 op_sel_hi:[0,0,0]
	v_mfma_scale_f32_16x16x128_f8f6f4 v[146:149], v[26:33], v[58:65], v[146:149], v1, v1 op_sel_hi:[0,0,0]
	v_mfma_scale_f32_16x16x128_f8f6f4 v[142:145], v[18:25], v[58:65], v[142:145], v1, v1 op_sel_hi:[0,0,0]
	v_mfma_scale_f32_16x16x128_f8f6f4 v[178:181], v[10:17], v[34:41], v[178:181], v1, v1 op_sel_hi:[0,0,0]
	v_mfma_scale_f32_16x16x128_f8f6f4 v[174:177], v[2:9], v[34:41], v[174:177], v1, v1 op_sel_hi:[0,0,0]
	v_lshl_add_u64 v[68:69], s[50:51], 0, v[210:211]
	s_add_i32 m0, s17, 0xe000
	s_nop 0
	global_load_lds_dwordx4 v[68:69], off
	v_mfma_scale_f32_16x16x128_f8f6f4 v[170:173], v[10:17], v[42:49], v[170:173], v1, v1 op_sel_hi:[0,0,0]
	v_mfma_scale_f32_16x16x128_f8f6f4 v[166:169], v[2:9], v[42:49], v[166:169], v1, v1 op_sel_hi:[0,0,0]
	v_mfma_scale_f32_16x16x128_f8f6f4 v[154:157], v[10:17], v[50:57], v[154:157], v1, v1 op_sel_hi:[0,0,0]
	v_mfma_scale_f32_16x16x128_f8f6f4 v[150:153], v[2:9], v[50:57], v[150:153], v1, v1 op_sel_hi:[0,0,0]
	v_mfma_scale_f32_16x16x128_f8f6f4 v[138:141], v[10:17], v[58:65], v[138:141], v1, v1 op_sel_hi:[0,0,0]
	v_mfma_scale_f32_16x16x128_f8f6f4 v[134:137], v[2:9], v[58:65], v[134:137], v1, v1 op_sel_hi:[0,0,0]
	s_barrier
	s_mov_b32 m0, s19
	v_lshl_add_u64 v[68:69], s[52:53], 0, v[200:201]
	global_load_lds_dwordx4 v[68:69], off
	v_lshl_add_u64 v[212:213], s[52:53], 0, v[204:205]
	s_mov_b32 m0, s33
	v_lshl_add_u64 v[68:69], v[68:69], 0, s[4:5]
	global_load_lds_dwordx4 v[212:213], off
	s_mov_b32 m0, s45
	s_nop 0
	global_load_lds_dwordx4 v[68:69], off
	v_lshl_add_u64 v[68:69], v[212:213], 0, s[4:5]
	s_mov_b32 m0, s47
	v_lshl_add_u64 v[212:213], s[54:55], 0, v[202:203]
	global_load_lds_dwordx4 v[68:69], off
	s_andn2_b64 vcc, exec, s[48:49]
	s_cbranch_vccnz .Lhalfskip_p8a
	ds_read_b128 v[58:61], v223 offset:16384
	ds_read_b128 v[62:65], v223 offset:17408
	ds_read_b128 v[50:53], v223 offset:18432
	ds_read_b128 v[54:57], v223 offset:19456
	ds_read_b128 v[42:45], v223 offset:20480
	ds_read_b128 v[46:49], v223 offset:21504
	ds_read_b128 v[34:37], v223 offset:22528
	ds_read_b128 v[38:41], v223 offset:23552
.Lhalfskip_p8a:
	v_cmp_ne_u32_e64 s[2:3], 1, v225
	s_waitcnt vmcnt(6)
	s_waitcnt lgkmcnt(0)
	s_barrier
	s_cbranch_vccnz .Lp8_skip_b
	s_waitcnt lgkmcnt(0)
	v_mfma_scale_f32_16x16x128_f8f6f4 v[130:133], v[26:33], v[58:65], v[130:133], v1, v1 op_sel_hi:[0,0,0]
	v_mfma_scale_f32_16x16x128_f8f6f4 v[126:129], v[18:25], v[58:65], v[126:129], v1, v1 op_sel_hi:[0,0,0]
	v_mfma_scale_f32_16x16x128_f8f6f4 v[114:117], v[26:33], v[50:57], v[114:117], v1, v1 op_sel_hi:[0,0,0]
	v_mfma_scale_f32_16x16x128_f8f6f4 v[110:113], v[18:25], v[50:57], v[110:113], v1, v1 op_sel_hi:[0,0,0]
	v_mfma_scale_f32_16x16x128_f8f6f4 v[98:101], v[26:33], v[42:49], v[98:101], v1, v1 op_sel_hi:[0,0,0]
	v_mfma_scale_f32_16x16x128_f8f6f4 v[94:97], v[18:25], v[42:49], v[94:97], v1, v1 op_sel_hi:[0,0,0]
	v_mfma_scale_f32_16x16x128_f8f6f4 v[82:85], v[26:33], v[34:41], v[82:85], v1, v1 op_sel_hi:[0,0,0]
	v_mfma_scale_f32_16x16x128_f8f6f4 v[78:81], v[18:25], v[34:41], v[78:81], v1, v1 op_sel_hi:[0,0,0]
	v_mfma_scale_f32_16x16x128_f8f6f4 v[122:125], v[10:17], v[58:65], v[122:125], v1, v1 op_sel_hi:[0,0,0]
	v_mfma_scale_f32_16x16x128_f8f6f4 v[118:121], v[2:9], v[58:65], v[118:121], v1, v1 op_sel_hi:[0,0,0]
	v_mfma_scale_f32_16x16x128_f8f6f4 v[106:109], v[10:17], v[50:57], v[106:109], v1, v1 op_sel_hi:[0,0,0]
	v_lshl_add_u64 v[68:69], s[54:55], 0, v[198:199]
	s_mov_b32 m0, s17
	s_nop 0
	global_load_lds_dwordx4 v[68:69], off
	v_mfma_scale_f32_16x16x128_f8f6f4 v[102:105], v[2:9], v[50:57], v[102:105], v1, v1 op_sel_hi:[0,0,0]
	v_mfma_scale_f32_16x16x128_f8f6f4 v[90:93], v[10:17], v[42:49], v[90:93], v1, v1 op_sel_hi:[0,0,0]
	s_mov_b32 m0, s58
	s_nop 0
	global_load_lds_dwordx4 v[212:213], off
	v_mfma_scale_f32_16x16x128_f8f6f4 v[86:89], v[2:9], v[42:49], v[86:89], v1, v1 op_sel_hi:[0,0,0]
	v_mfma_scale_f32_16x16x128_f8f6f4 v[74:77], v[10:17], v[34:41], v[74:77], v1, v1 op_sel_hi:[0,0,0]
	v_mfma_scale_f32_16x16x128_f8f6f4 v[70:73], v[2:9], v[34:41], v[70:73], v1, v1 op_sel_hi:[0,0,0]
.LBB0_903:
	s_add_u32 s56, s52, 0x40000
	s_addc_u32 s57, s53, 0
	s_barrier
	ds_read_b64_tr_b16 v[26:27], v215 offset:0
	ds_read_b64_tr_b16 v[28:29], v215 offset:1024
	ds_read_b64_tr_b16 v[30:31], v215 offset:8192
	ds_read_b64_tr_b16 v[32:33], v215 offset:9216
	ds_read_b64_tr_b16 v[18:19], v219 offset:0
	ds_read_b64_tr_b16 v[20:21], v219 offset:1024
	ds_read_b64_tr_b16 v[22:23], v219 offset:8192
	ds_read_b64_tr_b16 v[24:25], v219 offset:9216
	ds_read_b64_tr_b16 v[10:11], v216 offset:0
	ds_read_b64_tr_b16 v[12:13], v216 offset:1024
	ds_read_b64_tr_b16 v[14:15], v216 offset:8192
	ds_read_b64_tr_b16 v[16:17], v216 offset:9216
	ds_read_b64_tr_b16 v[2:3], v220 offset:0
	ds_read_b64_tr_b16 v[4:5], v220 offset:1024
	ds_read_b64_tr_b16 v[6:7], v220 offset:8192
	ds_read_b64_tr_b16 v[8:9], v220 offset:9216
	s_add_u32 s54, s54, 0x40000
	s_addc_u32 s55, s55, 0
	ds_read_b128 v[34:37], v223 offset:32768
	ds_read_b128 v[38:41], v223 offset:33792
	ds_read_b128 v[42:45], v223 offset:34816
	ds_read_b128 v[46:49], v223 offset:35840
	ds_read_b128 v[50:53], v223 offset:36864
	ds_read_b128 v[54:57], v223 offset:37888
	ds_read_b128 v[58:61], v223 offset:38912
	ds_read_b128 v[62:65], v223 offset:39936
	s_waitcnt vmcnt(6)
	s_waitcnt lgkmcnt(0)
	s_barrier
	s_waitcnt lgkmcnt(0)
	v_mfma_scale_f32_16x16x128_f8f6f4 v[194:197], v[26:33], v[34:41], v[194:197], v1, v1 op_sel_hi:[0,0,0]
	v_mfma_scale_f32_16x16x128_f8f6f4 v[190:193], v[18:25], v[34:41], v[190:193], v1, v1 op_sel_hi:[0,0,0]
	v_mfma_scale_f32_16x16x128_f8f6f4 v[186:189], v[26:33], v[42:49], v[186:189], v1, v1 op_sel_hi:[0,0,0]
	v_mfma_scale_f32_16x16x128_f8f6f4 v[182:185], v[18:25], v[42:49], v[182:185], v1, v1 op_sel_hi:[0,0,0]
	s_mov_b32 m0, s59
	v_lshl_add_u64 v[226:227], s[54:55], 0, v[198:199]
	global_load_lds_dwordx4 v[226:227], off
	v_mfma_scale_f32_16x16x128_f8f6f4 v[162:165], v[26:33], v[50:57], v[162:165], v1, v1 op_sel_hi:[0,0,0]
	v_mfma_scale_f32_16x16x128_f8f6f4 v[158:161], v[18:25], v[50:57], v[158:161], v1, v1 op_sel_hi:[0,0,0]
	v_mfma_scale_f32_16x16x128_f8f6f4 v[146:149], v[26:33], v[58:65], v[146:149], v1, v1 op_sel_hi:[0,0,0]
	v_mfma_scale_f32_16x16x128_f8f6f4 v[142:145], v[18:25], v[58:65], v[142:145], v1, v1 op_sel_hi:[0,0,0]
	v_mfma_scale_f32_16x16x128_f8f6f4 v[178:181], v[10:17], v[34:41], v[178:181], v1, v1 op_sel_hi:[0,0,0]
	v_mfma_scale_f32_16x16x128_f8f6f4 v[174:177], v[2:9], v[34:41], v[174:177], v1, v1 op_sel_hi:[0,0,0]
	v_lshl_add_u64 v[226:227], s[54:55], 0, v[202:203]
	s_mov_b32 m0, s60
	s_nop 0
	global_load_lds_dwordx4 v[226:227], off
	v_mfma_scale_f32_16x16x128_f8f6f4 v[170:173], v[10:17], v[42:49], v[170:173], v1, v1 op_sel_hi:[0,0,0]
	v_mfma_scale_f32_16x16x128_f8f6f4 v[166:169], v[2:9], v[42:49], v[166:169], v1, v1 op_sel_hi:[0,0,0]
	v_mfma_scale_f32_16x16x128_f8f6f4 v[154:157], v[10:17], v[50:57], v[154:157], v1, v1 op_sel_hi:[0,0,0]
	v_mfma_scale_f32_16x16x128_f8f6f4 v[150:153], v[2:9], v[50:57], v[150:153], v1, v1 op_sel_hi:[0,0,0]
	v_mfma_scale_f32_16x16x128_f8f6f4 v[138:141], v[10:17], v[58:65], v[138:141], v1, v1 op_sel_hi:[0,0,0]
	v_mfma_scale_f32_16x16x128_f8f6f4 v[134:137], v[2:9], v[58:65], v[134:137], v1, v1 op_sel_hi:[0,0,0]
	s_barrier
	v_lshl_add_u64 v[226:227], s[56:57], 0, v[200:201]
	s_add_i32 m0, s17, 0x18000
	s_nop 0
	global_load_lds_dwordx4 v[226:227], off
	s_add_i32 m0, s17, 0x1a000
	v_lshl_add_u64 v[226:227], s[56:57], 0, v[204:205]
	global_load_lds_dwordx4 v[226:227], off
	s_add_u32 s52, s52, 0x40100
	s_addc_u32 s53, s53, 0
	v_lshl_add_u64 v[226:227], s[52:53], 0, v[200:201]
	s_add_i32 m0, s17, 0x1c000
	v_lshl_add_u64 v[68:69], v[68:69], 0, s[12:13]
	global_load_lds_dwordx4 v[226:227], off
	v_lshl_add_u64 v[226:227], s[52:53], 0, v[204:205]
	s_add_i32 m0, s17, 0x1e000
	s_nop 0
	global_load_lds_dwordx4 v[226:227], off
	s_and_b64 vcc, exec, s[2:3]
	s_cbranch_vccnz .Lhalfskip_p8b
	ds_read_b128 v[58:61], v223 offset:49152
	ds_read_b128 v[62:65], v223 offset:50176
	ds_read_b128 v[50:53], v223 offset:51200
	ds_read_b128 v[54:57], v223 offset:52224
	ds_read_b128 v[42:45], v223 offset:53248
	ds_read_b128 v[46:49], v223 offset:54272
	ds_read_b128 v[34:37], v223 offset:55296
	ds_read_b128 v[38:41], v223 offset:56320
.Lhalfskip_p8b:
	s_waitcnt vmcnt(6)
	s_waitcnt lgkmcnt(0)
	s_barrier
	s_cbranch_vccnz .Lp8_skip_d
	s_waitcnt lgkmcnt(0)
	v_mfma_scale_f32_16x16x128_f8f6f4 v[130:133], v[26:33], v[58:65], v[130:133], v1, v1 op_sel_hi:[0,0,0]
	v_mfma_scale_f32_16x16x128_f8f6f4 v[126:129], v[18:25], v[58:65], v[126:129], v1, v1 op_sel_hi:[0,0,0]
	v_mfma_scale_f32_16x16x128_f8f6f4 v[114:117], v[26:33], v[50:57], v[114:117], v1, v1 op_sel_hi:[0,0,0]
	v_mfma_scale_f32_16x16x128_f8f6f4 v[110:113], v[18:25], v[50:57], v[110:113], v1, v1 op_sel_hi:[0,0,0]
	v_mfma_scale_f32_16x16x128_f8f6f4 v[98:101], v[26:33], v[42:49], v[98:101], v1, v1 op_sel_hi:[0,0,0]
	v_mfma_scale_f32_16x16x128_f8f6f4 v[94:97], v[18:25], v[42:49], v[94:97], v1, v1 op_sel_hi:[0,0,0]
	v_mfma_scale_f32_16x16x128_f8f6f4 v[82:85], v[26:33], v[34:41], v[82:85], v1, v1 op_sel_hi:[0,0,0]
	v_mfma_scale_f32_16x16x128_f8f6f4 v[78:81], v[18:25], v[34:41], v[78:81], v1, v1 op_sel_hi:[0,0,0]
	v_mfma_scale_f32_16x16x128_f8f6f4 v[122:125], v[10:17], v[58:65], v[122:125], v1, v1 op_sel_hi:[0,0,0]
	v_mfma_scale_f32_16x16x128_f8f6f4 v[118:121], v[2:9], v[58:65], v[118:121], v1, v1 op_sel_hi:[0,0,0]
	v_mfma_scale_f32_16x16x128_f8f6f4 v[106:109], v[10:17], v[50:57], v[106:109], v1, v1 op_sel_hi:[0,0,0]
	s_mov_b32 m0, s62
	s_nop 0
	global_load_lds_dwordx4 v[68:69], off
	v_mfma_scale_f32_16x16x128_f8f6f4 v[102:105], v[2:9], v[50:57], v[102:105], v1, v1 op_sel_hi:[0,0,0]
	v_mfma_scale_f32_16x16x128_f8f6f4 v[90:93], v[10:17], v[42:49], v[90:93], v1, v1 op_sel_hi:[0,0,0]
	v_lshl_add_u64 v[68:69], v[212:213], 0, s[12:13]
	s_mov_b32 m0, s63
	s_nop 0
	global_load_lds_dwordx4 v[68:69], off
	v_mfma_scale_f32_16x16x128_f8f6f4 v[86:89], v[2:9], v[42:49], v[86:89], v1, v1 op_sel_hi:[0,0,0]
	v_mfma_scale_f32_16x16x128_f8f6f4 v[74:77], v[10:17], v[34:41], v[74:77], v1, v1 op_sel_hi:[0,0,0]
	v_mfma_scale_f32_16x16x128_f8f6f4 v[70:73], v[2:9], v[34:41], v[70:73], v1, v1 op_sel_hi:[0,0,0]
	s_branch .LBB0_900

.LBB0_905:
	s_setprio 0
	s_and_b64 vcc, exec, s[14:15]
	s_cbranch_vccz .LBB0_907
	s_barrier
